# EpiRes (A3 bf16, A3 fp8, A5 fp8): the 16 residual-tile loads hoisted to the epilogue start in 1-3 batches with counted waits
# speedup vs baseline: 1.0006x; 1.0006x over previous
.LBB0_713:
	s_lshl_b32 s12, s11, 8
	s_lshl_b32 s8, s10, 8
	v_add_u32_e32 v132, s12, v139
	s_ashr_i32 s9, s8, 31
	v_ashrrev_i32_e32 v133, 31, v132
	v_mov_b32_e32 v131, s9
	v_or_b32_e32 v130, s8, v128
	v_lshlrev_b64 v[134:135], 11, v[132:133]
	v_lshl_add_u64 v[134:135], v[134:135], 0, v[130:131]
	v_lshl_add_u64 v[150:151], v[134:135], 1, s[4:5]
	global_load_dwordx4 v[146:149], v[150:151], off
	global_load_dwordx4 v[164:167], v[150:151], off offset:256
	v_add_u32_e32 v156, s12, v140
	v_ashrrev_i32_e32 v157, 31, v156
	v_lshlrev_b64 v[156:157], 11, v[156:157]
	v_lshl_add_u64 v[156:157], v[156:157], 0, v[130:131]
	v_lshl_add_u64 v[156:157], v[156:157], 1, s[4:5]
	global_load_dwordx4 v[174:177], v[156:157], off
	global_load_dwordx4 v[178:181], v[156:157], off offset:256
	v_add_u32_e32 v156, s12, v141
	v_ashrrev_i32_e32 v157, 31, v156
	v_lshlrev_b64 v[156:157], 11, v[156:157]
	v_lshl_add_u64 v[156:157], v[156:157], 0, v[130:131]
	v_lshl_add_u64 v[156:157], v[156:157], 1, s[4:5]
	global_load_dwordx4 v[182:185], v[156:157], off
	global_load_dwordx4 v[198:201], v[156:157], off offset:256
	v_add_u32_e32 v156, s12, v142
	v_ashrrev_i32_e32 v157, 31, v156
	v_lshlrev_b64 v[156:157], 11, v[156:157]
	v_lshl_add_u64 v[156:157], v[156:157], 0, v[130:131]
	v_lshl_add_u64 v[156:157], v[156:157], 1, s[4:5]
	global_load_dwordx4 v[202:205], v[156:157], off
	global_load_dwordx4 v[206:209], v[156:157], off offset:256
	v_add_u32_e32 v156, 0x80, v132
	v_ashrrev_i32_e32 v157, 31, v156
	v_lshlrev_b64 v[156:157], 11, v[156:157]
	v_lshl_add_u64 v[156:157], v[156:157], 0, v[130:131]
	v_lshl_add_u64 v[156:157], v[156:157], 1, s[4:5]
	global_load_dwordx4 v[210:213], v[156:157], off
	global_load_dwordx4 v[214:217], v[156:157], off offset:256
	v_add_u32_e32 v156, 0x90, v132
	v_ashrrev_i32_e32 v157, 31, v156
	v_lshlrev_b64 v[156:157], 11, v[156:157]
	v_lshl_add_u64 v[156:157], v[156:157], 0, v[130:131]
	v_lshl_add_u64 v[156:157], v[156:157], 1, s[4:5]
	global_load_dwordx4 v[224:227], v[156:157], off
	global_load_dwordx4 v[228:231], v[156:157], off offset:256
	v_add_u32_e32 v156, 0xa0, v132
	v_ashrrev_i32_e32 v157, 31, v156
	v_lshlrev_b64 v[156:157], 11, v[156:157]
	v_lshl_add_u64 v[156:157], v[156:157], 0, v[130:131]
	v_lshl_add_u64 v[156:157], v[156:157], 1, s[4:5]
	global_load_dwordx4 v[232:235], v[156:157], off
	global_load_dwordx4 v[236:239], v[156:157], off offset:256
	v_add_u32_e32 v156, 0xb0, v132
	v_ashrrev_i32_e32 v157, 31, v156
	v_lshlrev_b64 v[156:157], 11, v[156:157]
	v_lshl_add_u64 v[156:157], v[156:157], 0, v[130:131]
	v_lshl_add_u64 v[156:157], v[156:157], 1, s[4:5]
	global_load_dwordx4 v[240:243], v[156:157], off
	global_load_dwordx4 v[244:247], v[156:157], off offset:256
	v_mov_b32_e32 v161, v160
	v_cndmask_b32_e64 v145, 0, 1, s[16:17]
	v_cmp_ne_u32_e64 s[42:43], 1, v145
	s_andn2_b64 vcc, exec, s[16:17]
	s_mov_b64 s[74:75], s[96:97]
	s_waitcnt vmcnt(15)
	v_lshlrev_b32_e32 v152, 16, v146
	v_and_b32_e32 v153, 0xffff0000, v146
	v_lshlrev_b32_e32 v146, 16, v147
	v_and_b32_e32 v147, 0xffff0000, v147
	v_lshlrev_b32_e32 v154, 16, v148
	v_and_b32_e32 v155, 0xffff0000, v148
	v_lshlrev_b32_e32 v148, 16, v149
	v_and_b32_e32 v149, 0xffff0000, v149
	v_pk_fma_f32 v[126:127], v[160:161], v[126:127], v[146:147]
	v_pk_fma_f32 v[124:125], v[162:163], v[124:125], v[152:153]
	v_pk_fma_f32 v[122:123], v[160:161], v[122:123], v[148:149]
	v_pk_fma_f32 v[120:121], v[162:163], v[120:121], v[154:155]
	v_cvt_pk_bf16_f32 v146, v124, v125
	v_cvt_pk_bf16_f32 v147, v126, v127
	s_nop 0
	v_cvt_pk_bf16_f32 v148, v120, v121
	v_cvt_pk_bf16_f32 v149, v122, v123
	global_store_dwordx4 v[150:151], v[146:149], off
	s_cbranch_vccnz .LBB0_715
	s_nop 0
	v_mov_b32_e32 v146, v173
	v_mov_b32_e32 v147, v173
	v_cvt_pk_fp8_f32 v146, v124, v125
	v_cvt_pk_fp8_f32 v147, v120, v121
	v_readlane_b32 s8, v252, 21
	v_readlane_b32 s9, v252, 22
	v_cvt_pk_fp8_f32 v146, v126, v127 op_sel:[0,0,1]
	v_cvt_pk_fp8_f32 v147, v122, v123 op_sel:[0,0,1]
	v_lshl_add_u64 v[148:149], s[8:9], 0, v[134:135]
	global_store_dwordx2 v[148:149], v[146:147], off
.LBB0_715:
	v_or_b32_e32 v134, 0x80, v134
	v_lshl_add_u64 v[150:151], v[134:135], 1, s[4:5]
	s_nop 0
	s_and_b64 vcc, exec, s[42:43]
	s_waitcnt vmcnt(15)
	v_mov_b32_e32 v146, v164
	v_mov_b32_e32 v147, v165
	v_mov_b32_e32 v148, v166
	v_mov_b32_e32 v149, v167
	v_lshlrev_b32_e32 v152, 16, v146
	v_and_b32_e32 v153, 0xffff0000, v146
	v_lshlrev_b32_e32 v146, 16, v147
	v_and_b32_e32 v147, 0xffff0000, v147
	v_lshlrev_b32_e32 v154, 16, v148
	v_and_b32_e32 v155, 0xffff0000, v148
	v_lshlrev_b32_e32 v148, 16, v149
	v_and_b32_e32 v149, 0xffff0000, v149
	v_pk_fma_f32 v[118:119], v[160:161], v[118:119], v[146:147]
	v_pk_fma_f32 v[116:117], v[162:163], v[116:117], v[152:153]
	v_pk_fma_f32 v[114:115], v[160:161], v[114:115], v[148:149]
	v_pk_fma_f32 v[112:113], v[162:163], v[112:113], v[154:155]
	v_cvt_pk_bf16_f32 v146, v116, v117
	v_cvt_pk_bf16_f32 v147, v118, v119
	s_nop 0
	v_cvt_pk_bf16_f32 v148, v112, v113
	v_cvt_pk_bf16_f32 v149, v114, v115
	global_store_dwordx4 v[150:151], v[146:149], off
	s_cbranch_vccnz .LBB0_717
	s_nop 0
	v_mov_b32_e32 v146, v173
	v_mov_b32_e32 v147, v173
	v_cvt_pk_fp8_f32 v146, v116, v117
	v_cvt_pk_fp8_f32 v147, v112, v113
	v_readlane_b32 s8, v252, 21
	v_readlane_b32 s9, v252, 22
	v_cvt_pk_fp8_f32 v146, v118, v119 op_sel:[0,0,1]
	v_cvt_pk_fp8_f32 v147, v114, v115 op_sel:[0,0,1]
	v_lshl_add_u64 v[134:135], s[8:9], 0, v[134:135]
	global_store_dwordx2 v[134:135], v[146:147], off

.LBB0_719:
	s_or_b64 exec, exec, s[10:11]
	v_add_u32_e32 v112, s12, v140
	s_waitcnt lgkmcnt(0)
	v_ashrrev_i32_e32 v113, 31, v112
	v_lshlrev_b64 v[114:115], 11, v[112:113]
	v_lshl_add_u64 v[114:115], v[114:115], 0, v[130:131]
	v_lshl_add_u64 v[122:123], v[114:115], 1, s[4:5]
	s_nop 0
	v_mov_b32_e32 v161, v160
	s_and_b64 vcc, exec, s[42:43]
	s_waitcnt vmcnt(15)
	v_mov_b32_e32 v118, v174
	v_mov_b32_e32 v119, v175
	v_mov_b32_e32 v120, v176
	v_mov_b32_e32 v121, v177
	v_lshlrev_b32_e32 v124, 16, v118
	v_and_b32_e32 v125, 0xffff0000, v118
	v_lshlrev_b32_e32 v118, 16, v119
	v_and_b32_e32 v119, 0xffff0000, v119
	v_lshlrev_b32_e32 v126, 16, v120
	v_and_b32_e32 v127, 0xffff0000, v120
	v_lshlrev_b32_e32 v120, 16, v121
	v_and_b32_e32 v121, 0xffff0000, v121
	v_pk_fma_f32 v[110:111], v[160:161], v[110:111], v[118:119]
	v_pk_fma_f32 v[108:109], v[162:163], v[108:109], v[124:125]
	v_pk_fma_f32 v[106:107], v[160:161], v[106:107], v[120:121]
	v_pk_fma_f32 v[104:105], v[162:163], v[104:105], v[126:127]
	v_cvt_pk_bf16_f32 v118, v108, v109
	v_cvt_pk_bf16_f32 v119, v110, v111
	s_nop 0
	v_cvt_pk_bf16_f32 v120, v104, v105
	v_cvt_pk_bf16_f32 v121, v106, v107
	global_store_dwordx4 v[122:123], v[118:121], off
	s_cbranch_vccnz .LBB0_721
	s_nop 0
	v_mov_b32_e32 v118, v173
	v_mov_b32_e32 v119, v173
	v_cvt_pk_fp8_f32 v118, v108, v109
	v_cvt_pk_fp8_f32 v119, v104, v105
	v_readlane_b32 s10, v252, 21
	v_readlane_b32 s11, v252, 22
	v_cvt_pk_fp8_f32 v118, v110, v111 op_sel:[0,0,1]
	v_cvt_pk_fp8_f32 v119, v106, v107 op_sel:[0,0,1]
	v_lshl_add_u64 v[120:121], s[10:11], 0, v[114:115]
	global_store_dwordx2 v[120:121], v[118:119], off
.LBB0_721:
	v_or_b32_e32 v114, 0x80, v114
	v_lshl_add_u64 v[122:123], v[114:115], 1, s[4:5]
	s_nop 0
	s_and_b64 vcc, exec, s[42:43]
	s_waitcnt vmcnt(15)
	v_mov_b32_e32 v118, v178
	v_mov_b32_e32 v119, v179
	v_mov_b32_e32 v120, v180
	v_mov_b32_e32 v121, v181
	v_lshlrev_b32_e32 v124, 16, v118
	v_and_b32_e32 v125, 0xffff0000, v118
	v_lshlrev_b32_e32 v118, 16, v119
	v_and_b32_e32 v119, 0xffff0000, v119
	v_lshlrev_b32_e32 v126, 16, v120
	v_and_b32_e32 v127, 0xffff0000, v120
	v_lshlrev_b32_e32 v120, 16, v121
	v_and_b32_e32 v121, 0xffff0000, v121
	v_pk_fma_f32 v[102:103], v[160:161], v[102:103], v[118:119]
	v_pk_fma_f32 v[100:101], v[162:163], v[100:101], v[124:125]
	v_pk_fma_f32 v[98:99], v[160:161], v[98:99], v[120:121]
	v_pk_fma_f32 v[96:97], v[162:163], v[96:97], v[126:127]
	v_cvt_pk_bf16_f32 v118, v100, v101
	v_cvt_pk_bf16_f32 v119, v102, v103
	s_nop 0
	v_cvt_pk_bf16_f32 v120, v96, v97
	v_cvt_pk_bf16_f32 v121, v98, v99
	global_store_dwordx4 v[122:123], v[118:121], off
	s_cbranch_vccnz .LBB0_723
	s_nop 0
	v_mov_b32_e32 v118, v173
	v_mov_b32_e32 v119, v173
	v_cvt_pk_fp8_f32 v118, v100, v101
	v_cvt_pk_fp8_f32 v119, v96, v97
	v_readlane_b32 s10, v252, 21
	v_readlane_b32 s11, v252, 22
	v_cvt_pk_fp8_f32 v118, v102, v103 op_sel:[0,0,1]
	v_cvt_pk_fp8_f32 v119, v98, v99 op_sel:[0,0,1]
	v_lshl_add_u64 v[114:115], s[10:11], 0, v[114:115]
	global_store_dwordx2 v[114:115], v[118:119], off

.LBB0_725:
	s_or_b64 exec, exec, s[10:11]
	v_add_u32_e32 v96, s12, v141
	s_waitcnt lgkmcnt(0)
	v_ashrrev_i32_e32 v97, 31, v96
	v_lshlrev_b64 v[98:99], 11, v[96:97]
	v_lshl_add_u64 v[98:99], v[98:99], 0, v[130:131]
	v_lshl_add_u64 v[104:105], v[98:99], 1, s[4:5]
	s_nop 0
	v_mov_b32_e32 v161, v160
	s_and_b64 vcc, exec, s[42:43]
	s_waitcnt vmcnt(15)
	v_mov_b32_e32 v100, v182
	v_mov_b32_e32 v101, v183
	v_mov_b32_e32 v102, v184
	v_mov_b32_e32 v103, v185
	v_lshlrev_b32_e32 v106, 16, v100
	v_and_b32_e32 v107, 0xffff0000, v100
	v_lshlrev_b32_e32 v100, 16, v101
	v_and_b32_e32 v101, 0xffff0000, v101
	v_lshlrev_b32_e32 v108, 16, v102
	v_and_b32_e32 v109, 0xffff0000, v102
	v_lshlrev_b32_e32 v102, 16, v103
	v_and_b32_e32 v103, 0xffff0000, v103
	v_pk_fma_f32 v[94:95], v[160:161], v[94:95], v[100:101]
	v_pk_fma_f32 v[92:93], v[162:163], v[92:93], v[106:107]
	v_pk_fma_f32 v[90:91], v[160:161], v[90:91], v[102:103]
	v_pk_fma_f32 v[88:89], v[162:163], v[88:89], v[108:109]
	v_cvt_pk_bf16_f32 v100, v92, v93
	v_cvt_pk_bf16_f32 v101, v94, v95
	s_nop 0
	v_cvt_pk_bf16_f32 v102, v88, v89
	v_cvt_pk_bf16_f32 v103, v90, v91
	global_store_dwordx4 v[104:105], v[100:103], off
	s_cbranch_vccnz .LBB0_727
	s_nop 0
	v_mov_b32_e32 v100, v173
	v_mov_b32_e32 v101, v173
	v_cvt_pk_fp8_f32 v100, v92, v93
	v_cvt_pk_fp8_f32 v101, v88, v89
	v_readlane_b32 s10, v252, 21
	v_readlane_b32 s11, v252, 22
	v_cvt_pk_fp8_f32 v100, v94, v95 op_sel:[0,0,1]
	v_cvt_pk_fp8_f32 v101, v90, v91 op_sel:[0,0,1]
	v_lshl_add_u64 v[102:103], s[10:11], 0, v[98:99]
	global_store_dwordx2 v[102:103], v[100:101], off
.LBB0_727:
	v_or_b32_e32 v98, 0x80, v98
	v_lshl_add_u64 v[104:105], v[98:99], 1, s[4:5]
	s_nop 0
	s_and_b64 vcc, exec, s[42:43]
	s_waitcnt vmcnt(15)
	v_mov_b32_e32 v100, v198
	v_mov_b32_e32 v101, v199
	v_mov_b32_e32 v102, v200
	v_mov_b32_e32 v103, v201
	v_lshlrev_b32_e32 v106, 16, v100
	v_and_b32_e32 v107, 0xffff0000, v100
	v_lshlrev_b32_e32 v100, 16, v101
	v_and_b32_e32 v101, 0xffff0000, v101
	v_lshlrev_b32_e32 v108, 16, v102
	v_and_b32_e32 v109, 0xffff0000, v102
	v_lshlrev_b32_e32 v102, 16, v103
	v_and_b32_e32 v103, 0xffff0000, v103
	v_pk_fma_f32 v[86:87], v[160:161], v[86:87], v[100:101]
	v_pk_fma_f32 v[84:85], v[162:163], v[84:85], v[106:107]
	v_pk_fma_f32 v[82:83], v[160:161], v[82:83], v[102:103]
	v_pk_fma_f32 v[80:81], v[162:163], v[80:81], v[108:109]
	v_cvt_pk_bf16_f32 v100, v84, v85
	v_cvt_pk_bf16_f32 v101, v86, v87
	s_nop 0
	v_cvt_pk_bf16_f32 v102, v80, v81
	v_cvt_pk_bf16_f32 v103, v82, v83
	global_store_dwordx4 v[104:105], v[100:103], off
	s_cbranch_vccnz .LBB0_729
	s_nop 0
	v_mov_b32_e32 v100, v173
	v_mov_b32_e32 v101, v173
	v_cvt_pk_fp8_f32 v100, v84, v85
	v_cvt_pk_fp8_f32 v101, v80, v81
	v_readlane_b32 s10, v252, 21
	v_readlane_b32 s11, v252, 22
	v_cvt_pk_fp8_f32 v100, v86, v87 op_sel:[0,0,1]
	v_cvt_pk_fp8_f32 v101, v82, v83 op_sel:[0,0,1]
	v_lshl_add_u64 v[98:99], s[10:11], 0, v[98:99]
	global_store_dwordx2 v[98:99], v[100:101], off

.LBB0_731:
	s_or_b64 exec, exec, s[10:11]
	v_add_u32_e32 v80, s12, v142
	s_waitcnt lgkmcnt(0)
	v_ashrrev_i32_e32 v81, 31, v80
	v_lshlrev_b64 v[82:83], 11, v[80:81]
	v_lshl_add_u64 v[82:83], v[82:83], 0, v[130:131]
	v_lshl_add_u64 v[88:89], v[82:83], 1, s[4:5]
	s_nop 0
	v_mov_b32_e32 v161, v160
	s_and_b64 vcc, exec, s[42:43]
	s_waitcnt vmcnt(15)
	v_mov_b32_e32 v84, v202
	v_mov_b32_e32 v85, v203
	v_mov_b32_e32 v86, v204
	v_mov_b32_e32 v87, v205
	v_lshlrev_b32_e32 v90, 16, v84
	v_and_b32_e32 v91, 0xffff0000, v84
	v_lshlrev_b32_e32 v84, 16, v85
	v_and_b32_e32 v85, 0xffff0000, v85
	v_lshlrev_b32_e32 v92, 16, v86
	v_and_b32_e32 v93, 0xffff0000, v86
	v_lshlrev_b32_e32 v86, 16, v87
	v_and_b32_e32 v87, 0xffff0000, v87
	v_pk_fma_f32 v[78:79], v[160:161], v[78:79], v[84:85]
	v_pk_fma_f32 v[76:77], v[162:163], v[76:77], v[90:91]
	v_pk_fma_f32 v[74:75], v[160:161], v[74:75], v[86:87]
	v_pk_fma_f32 v[72:73], v[162:163], v[72:73], v[92:93]
	v_cvt_pk_bf16_f32 v84, v76, v77
	v_cvt_pk_bf16_f32 v85, v78, v79
	s_nop 0
	v_cvt_pk_bf16_f32 v86, v72, v73
	v_cvt_pk_bf16_f32 v87, v74, v75
	global_store_dwordx4 v[88:89], v[84:87], off
	s_cbranch_vccnz .LBB0_733
	s_nop 0
	v_mov_b32_e32 v84, v173
	v_mov_b32_e32 v85, v173
	v_cvt_pk_fp8_f32 v84, v76, v77
	v_cvt_pk_fp8_f32 v85, v72, v73
	v_readlane_b32 s10, v252, 21
	v_readlane_b32 s11, v252, 22
	v_cvt_pk_fp8_f32 v84, v78, v79 op_sel:[0,0,1]
	v_cvt_pk_fp8_f32 v85, v74, v75 op_sel:[0,0,1]
	v_lshl_add_u64 v[86:87], s[10:11], 0, v[82:83]
	global_store_dwordx2 v[86:87], v[84:85], off
.LBB0_733:
	v_or_b32_e32 v82, 0x80, v82
	v_lshl_add_u64 v[88:89], v[82:83], 1, s[4:5]
	s_nop 0
	s_and_b64 vcc, exec, s[42:43]
	s_waitcnt vmcnt(15)
	v_mov_b32_e32 v84, v206
	v_mov_b32_e32 v85, v207
	v_mov_b32_e32 v86, v208
	v_mov_b32_e32 v87, v209
	v_lshlrev_b32_e32 v90, 16, v84
	v_and_b32_e32 v91, 0xffff0000, v84
	v_lshlrev_b32_e32 v84, 16, v85
	v_and_b32_e32 v85, 0xffff0000, v85
	v_lshlrev_b32_e32 v92, 16, v86
	v_and_b32_e32 v93, 0xffff0000, v86
	v_lshlrev_b32_e32 v86, 16, v87
	v_and_b32_e32 v87, 0xffff0000, v87
	v_pk_fma_f32 v[70:71], v[160:161], v[70:71], v[84:85]
	v_pk_fma_f32 v[68:69], v[162:163], v[68:69], v[90:91]
	v_pk_fma_f32 v[66:67], v[160:161], v[66:67], v[86:87]
	v_pk_fma_f32 v[64:65], v[162:163], v[64:65], v[92:93]
	v_cvt_pk_bf16_f32 v84, v68, v69
	v_cvt_pk_bf16_f32 v85, v70, v71
	s_nop 0
	v_cvt_pk_bf16_f32 v86, v64, v65
	v_cvt_pk_bf16_f32 v87, v66, v67
	global_store_dwordx4 v[88:89], v[84:87], off
	s_cbranch_vccnz .LBB0_735
	s_nop 0
	v_mov_b32_e32 v84, v173
	v_mov_b32_e32 v85, v173
	v_cvt_pk_fp8_f32 v84, v68, v69
	v_cvt_pk_fp8_f32 v85, v64, v65
	v_readlane_b32 s10, v252, 21
	v_readlane_b32 s11, v252, 22
	v_cvt_pk_fp8_f32 v84, v70, v71 op_sel:[0,0,1]
	v_cvt_pk_fp8_f32 v85, v66, v67 op_sel:[0,0,1]
	v_lshl_add_u64 v[82:83], s[10:11], 0, v[82:83]
	global_store_dwordx2 v[82:83], v[84:85], off

.LBB0_737:
	s_or_b64 exec, exec, s[10:11]
	v_add_u32_e32 v64, 0x80, v132
	s_waitcnt lgkmcnt(0)
	v_ashrrev_i32_e32 v65, 31, v64
	v_lshlrev_b64 v[66:67], 11, v[64:65]
	v_lshl_add_u64 v[66:67], v[66:67], 0, v[130:131]
	v_lshl_add_u64 v[72:73], v[66:67], 1, s[4:5]
	s_nop 0
	v_mov_b32_e32 v161, v160
	s_and_b64 vcc, exec, s[42:43]
	s_waitcnt vmcnt(15)
	v_mov_b32_e32 v68, v210
	v_mov_b32_e32 v69, v211
	v_mov_b32_e32 v70, v212
	v_mov_b32_e32 v71, v213
	v_lshlrev_b32_e32 v74, 16, v68
	v_and_b32_e32 v75, 0xffff0000, v68
	v_lshlrev_b32_e32 v68, 16, v69
	v_and_b32_e32 v69, 0xffff0000, v69
	v_lshlrev_b32_e32 v76, 16, v70
	v_and_b32_e32 v77, 0xffff0000, v70
	v_lshlrev_b32_e32 v70, 16, v71
	v_and_b32_e32 v71, 0xffff0000, v71
	v_pk_fma_f32 v[62:63], v[160:161], v[62:63], v[68:69]
	v_pk_fma_f32 v[60:61], v[162:163], v[60:61], v[74:75]
	v_pk_fma_f32 v[58:59], v[160:161], v[58:59], v[70:71]
	v_pk_fma_f32 v[56:57], v[162:163], v[56:57], v[76:77]
	v_cvt_pk_bf16_f32 v68, v60, v61
	v_cvt_pk_bf16_f32 v69, v62, v63
	s_nop 0
	v_cvt_pk_bf16_f32 v70, v56, v57
	v_cvt_pk_bf16_f32 v71, v58, v59
	global_store_dwordx4 v[72:73], v[68:71], off
	s_cbranch_vccnz .LBB0_739
	s_nop 0
	v_mov_b32_e32 v68, v173
	v_mov_b32_e32 v69, v173
	v_cvt_pk_fp8_f32 v68, v60, v61
	v_cvt_pk_fp8_f32 v69, v56, v57
	v_readlane_b32 s10, v252, 21
	v_readlane_b32 s11, v252, 22
	v_cvt_pk_fp8_f32 v68, v62, v63 op_sel:[0,0,1]
	v_cvt_pk_fp8_f32 v69, v58, v59 op_sel:[0,0,1]
	v_lshl_add_u64 v[70:71], s[10:11], 0, v[66:67]
	global_store_dwordx2 v[70:71], v[68:69], off
.LBB0_739:
	v_or_b32_e32 v66, 0x80, v66
	v_lshl_add_u64 v[72:73], v[66:67], 1, s[4:5]
	s_nop 0
	s_and_b64 vcc, exec, s[42:43]
	s_waitcnt vmcnt(15)
	v_mov_b32_e32 v68, v214
	v_mov_b32_e32 v69, v215
	v_mov_b32_e32 v70, v216
	v_mov_b32_e32 v71, v217
	v_lshlrev_b32_e32 v74, 16, v68
	v_and_b32_e32 v75, 0xffff0000, v68
	v_lshlrev_b32_e32 v68, 16, v69
	v_and_b32_e32 v69, 0xffff0000, v69
	v_lshlrev_b32_e32 v76, 16, v70
	v_and_b32_e32 v77, 0xffff0000, v70
	v_lshlrev_b32_e32 v70, 16, v71
	v_and_b32_e32 v71, 0xffff0000, v71
	v_pk_fma_f32 v[54:55], v[160:161], v[54:55], v[68:69]
	v_pk_fma_f32 v[52:53], v[162:163], v[52:53], v[74:75]
	v_pk_fma_f32 v[50:51], v[160:161], v[50:51], v[70:71]
	v_pk_fma_f32 v[48:49], v[162:163], v[48:49], v[76:77]
	v_cvt_pk_bf16_f32 v68, v52, v53
	v_cvt_pk_bf16_f32 v69, v54, v55
	s_nop 0
	v_cvt_pk_bf16_f32 v70, v48, v49
	v_cvt_pk_bf16_f32 v71, v50, v51
	global_store_dwordx4 v[72:73], v[68:71], off
	s_cbranch_vccnz .LBB0_741
	s_nop 0
	v_mov_b32_e32 v68, v173
	v_mov_b32_e32 v69, v173
	v_cvt_pk_fp8_f32 v68, v52, v53
	v_cvt_pk_fp8_f32 v69, v48, v49
	v_readlane_b32 s10, v252, 21
	v_readlane_b32 s11, v252, 22
	v_cvt_pk_fp8_f32 v68, v54, v55 op_sel:[0,0,1]
	v_cvt_pk_fp8_f32 v69, v50, v51 op_sel:[0,0,1]
	v_lshl_add_u64 v[66:67], s[10:11], 0, v[66:67]
	global_store_dwordx2 v[66:67], v[68:69], off

.LBB0_743:
	s_or_b64 exec, exec, s[10:11]
	v_add_u32_e32 v48, 0x90, v132
	s_waitcnt lgkmcnt(0)
	v_ashrrev_i32_e32 v49, 31, v48
	v_lshlrev_b64 v[50:51], 11, v[48:49]
	v_lshl_add_u64 v[50:51], v[50:51], 0, v[130:131]
	v_lshl_add_u64 v[56:57], v[50:51], 1, s[4:5]
	s_nop 0
	v_mov_b32_e32 v161, v160
	s_and_b64 vcc, exec, s[42:43]
	s_waitcnt vmcnt(15)
	v_mov_b32_e32 v52, v224
	v_mov_b32_e32 v53, v225
	v_mov_b32_e32 v54, v226
	v_mov_b32_e32 v55, v227
	v_lshlrev_b32_e32 v58, 16, v52
	v_and_b32_e32 v59, 0xffff0000, v52
	v_lshlrev_b32_e32 v52, 16, v53
	v_and_b32_e32 v53, 0xffff0000, v53
	v_lshlrev_b32_e32 v60, 16, v54
	v_and_b32_e32 v61, 0xffff0000, v54
	v_lshlrev_b32_e32 v54, 16, v55
	v_and_b32_e32 v55, 0xffff0000, v55
	v_pk_fma_f32 v[46:47], v[160:161], v[46:47], v[52:53]
	v_pk_fma_f32 v[44:45], v[162:163], v[44:45], v[58:59]
	v_pk_fma_f32 v[42:43], v[160:161], v[42:43], v[54:55]
	v_pk_fma_f32 v[40:41], v[162:163], v[40:41], v[60:61]
	v_cvt_pk_bf16_f32 v52, v44, v45
	v_cvt_pk_bf16_f32 v53, v46, v47
	s_nop 0
	v_cvt_pk_bf16_f32 v54, v40, v41
	v_cvt_pk_bf16_f32 v55, v42, v43
	global_store_dwordx4 v[56:57], v[52:55], off
	s_cbranch_vccnz .LBB0_745
	s_nop 0
	v_mov_b32_e32 v52, v173
	v_mov_b32_e32 v53, v173
	v_cvt_pk_fp8_f32 v52, v44, v45
	v_cvt_pk_fp8_f32 v53, v40, v41
	v_readlane_b32 s10, v252, 21
	v_readlane_b32 s11, v252, 22
	v_cvt_pk_fp8_f32 v52, v46, v47 op_sel:[0,0,1]
	v_cvt_pk_fp8_f32 v53, v42, v43 op_sel:[0,0,1]
	v_lshl_add_u64 v[54:55], s[10:11], 0, v[50:51]
	global_store_dwordx2 v[54:55], v[52:53], off
.LBB0_745:
	v_or_b32_e32 v50, 0x80, v50
	v_lshl_add_u64 v[56:57], v[50:51], 1, s[4:5]
	s_nop 0
	s_and_b64 vcc, exec, s[42:43]
	s_waitcnt vmcnt(15)
	v_mov_b32_e32 v52, v228
	v_mov_b32_e32 v53, v229
	v_mov_b32_e32 v54, v230
	v_mov_b32_e32 v55, v231
	v_lshlrev_b32_e32 v58, 16, v52
	v_and_b32_e32 v59, 0xffff0000, v52
	v_lshlrev_b32_e32 v52, 16, v53
	v_and_b32_e32 v53, 0xffff0000, v53
	v_lshlrev_b32_e32 v60, 16, v54
	v_and_b32_e32 v61, 0xffff0000, v54
	v_lshlrev_b32_e32 v54, 16, v55
	v_and_b32_e32 v55, 0xffff0000, v55
	v_pk_fma_f32 v[38:39], v[160:161], v[38:39], v[52:53]
	v_pk_fma_f32 v[36:37], v[162:163], v[36:37], v[58:59]
	v_pk_fma_f32 v[34:35], v[160:161], v[34:35], v[54:55]
	v_pk_fma_f32 v[32:33], v[162:163], v[32:33], v[60:61]
	v_cvt_pk_bf16_f32 v52, v36, v37
	v_cvt_pk_bf16_f32 v53, v38, v39
	s_nop 0
	v_cvt_pk_bf16_f32 v54, v32, v33
	v_cvt_pk_bf16_f32 v55, v34, v35
	global_store_dwordx4 v[56:57], v[52:55], off
	s_cbranch_vccnz .LBB0_747
	s_nop 0
	v_mov_b32_e32 v52, v173
	v_mov_b32_e32 v53, v173
	v_cvt_pk_fp8_f32 v52, v36, v37
	v_cvt_pk_fp8_f32 v53, v32, v33
	v_readlane_b32 s10, v252, 21
	v_readlane_b32 s11, v252, 22
	v_cvt_pk_fp8_f32 v52, v38, v39 op_sel:[0,0,1]
	v_cvt_pk_fp8_f32 v53, v34, v35 op_sel:[0,0,1]
	v_lshl_add_u64 v[50:51], s[10:11], 0, v[50:51]
	global_store_dwordx2 v[50:51], v[52:53], off

.LBB0_749:
	s_or_b64 exec, exec, s[10:11]
	v_add_u32_e32 v32, 0xa0, v132
	s_waitcnt lgkmcnt(0)
	v_ashrrev_i32_e32 v33, 31, v32
	v_lshlrev_b64 v[34:35], 11, v[32:33]
	v_lshl_add_u64 v[34:35], v[34:35], 0, v[130:131]
	v_lshl_add_u64 v[40:41], v[34:35], 1, s[4:5]
	s_nop 0
	v_mov_b32_e32 v161, v160
	s_and_b64 vcc, exec, s[42:43]
	s_waitcnt vmcnt(15)
	v_mov_b32_e32 v36, v232
	v_mov_b32_e32 v37, v233
	v_mov_b32_e32 v38, v234
	v_mov_b32_e32 v39, v235
	v_lshlrev_b32_e32 v42, 16, v36
	v_and_b32_e32 v43, 0xffff0000, v36
	v_lshlrev_b32_e32 v36, 16, v37
	v_and_b32_e32 v37, 0xffff0000, v37
	v_lshlrev_b32_e32 v44, 16, v38
	v_and_b32_e32 v45, 0xffff0000, v38
	v_lshlrev_b32_e32 v38, 16, v39
	v_and_b32_e32 v39, 0xffff0000, v39
	v_pk_fma_f32 v[30:31], v[160:161], v[30:31], v[36:37]
	v_pk_fma_f32 v[28:29], v[162:163], v[28:29], v[42:43]
	v_pk_fma_f32 v[26:27], v[160:161], v[26:27], v[38:39]
	v_pk_fma_f32 v[24:25], v[162:163], v[24:25], v[44:45]
	v_cvt_pk_bf16_f32 v36, v28, v29
	v_cvt_pk_bf16_f32 v37, v30, v31
	s_nop 0
	v_cvt_pk_bf16_f32 v38, v24, v25
	v_cvt_pk_bf16_f32 v39, v26, v27
	global_store_dwordx4 v[40:41], v[36:39], off
	s_cbranch_vccnz .LBB0_751
	s_nop 0
	v_mov_b32_e32 v36, v173
	v_mov_b32_e32 v37, v173
	v_cvt_pk_fp8_f32 v36, v28, v29
	v_cvt_pk_fp8_f32 v37, v24, v25
	v_readlane_b32 s10, v252, 21
	v_readlane_b32 s11, v252, 22
	v_cvt_pk_fp8_f32 v36, v30, v31 op_sel:[0,0,1]
	v_cvt_pk_fp8_f32 v37, v26, v27 op_sel:[0,0,1]
	v_lshl_add_u64 v[38:39], s[10:11], 0, v[34:35]
	global_store_dwordx2 v[38:39], v[36:37], off
.LBB0_751:
	v_or_b32_e32 v34, 0x80, v34
	v_lshl_add_u64 v[40:41], v[34:35], 1, s[4:5]
	s_nop 0
	s_and_b64 vcc, exec, s[42:43]
	s_waitcnt vmcnt(15)
	v_mov_b32_e32 v36, v236
	v_mov_b32_e32 v37, v237
	v_mov_b32_e32 v38, v238
	v_mov_b32_e32 v39, v239
	v_lshlrev_b32_e32 v42, 16, v36
	v_and_b32_e32 v43, 0xffff0000, v36
	v_lshlrev_b32_e32 v36, 16, v37
	v_and_b32_e32 v37, 0xffff0000, v37
	v_lshlrev_b32_e32 v44, 16, v38
	v_and_b32_e32 v45, 0xffff0000, v38
	v_lshlrev_b32_e32 v38, 16, v39
	v_and_b32_e32 v39, 0xffff0000, v39
	v_pk_fma_f32 v[22:23], v[160:161], v[22:23], v[36:37]
	v_pk_fma_f32 v[20:21], v[162:163], v[20:21], v[42:43]
	v_pk_fma_f32 v[18:19], v[160:161], v[18:19], v[38:39]
	v_pk_fma_f32 v[16:17], v[162:163], v[16:17], v[44:45]
	v_cvt_pk_bf16_f32 v36, v20, v21
	v_cvt_pk_bf16_f32 v37, v22, v23
	s_nop 0
	v_cvt_pk_bf16_f32 v38, v16, v17
	v_cvt_pk_bf16_f32 v39, v18, v19
	global_store_dwordx4 v[40:41], v[36:39], off
	s_cbranch_vccnz .LBB0_753
	s_nop 0
	v_mov_b32_e32 v36, v173
	v_mov_b32_e32 v37, v173
	v_cvt_pk_fp8_f32 v36, v20, v21
	v_cvt_pk_fp8_f32 v37, v16, v17
	v_readlane_b32 s10, v252, 21
	v_readlane_b32 s11, v252, 22
	v_cvt_pk_fp8_f32 v36, v22, v23 op_sel:[0,0,1]
	v_cvt_pk_fp8_f32 v37, v18, v19 op_sel:[0,0,1]
	v_lshl_add_u64 v[34:35], s[10:11], 0, v[34:35]
	global_store_dwordx2 v[34:35], v[36:37], off

.LBB0_755:
	s_or_b64 exec, exec, s[10:11]
	v_add_u32_e32 v16, 0xb0, v132
	s_waitcnt lgkmcnt(0)
	v_ashrrev_i32_e32 v17, 31, v16
	v_lshlrev_b64 v[18:19], 11, v[16:17]
	v_lshl_add_u64 v[18:19], v[18:19], 0, v[130:131]
	v_lshl_add_u64 v[24:25], v[18:19], 1, s[4:5]
	s_nop 0
	v_mov_b32_e32 v161, v160
	s_and_b64 vcc, exec, s[42:43]
	s_waitcnt vmcnt(15)
	v_mov_b32_e32 v20, v240
	v_mov_b32_e32 v21, v241
	v_mov_b32_e32 v22, v242
	v_mov_b32_e32 v23, v243
	v_lshlrev_b32_e32 v26, 16, v20
	v_and_b32_e32 v27, 0xffff0000, v20
	v_lshlrev_b32_e32 v20, 16, v21
	v_and_b32_e32 v21, 0xffff0000, v21
	v_lshlrev_b32_e32 v28, 16, v22
	v_and_b32_e32 v29, 0xffff0000, v22
	v_lshlrev_b32_e32 v22, 16, v23
	v_and_b32_e32 v23, 0xffff0000, v23
	v_pk_fma_f32 v[14:15], v[160:161], v[14:15], v[20:21]
	v_pk_fma_f32 v[12:13], v[162:163], v[12:13], v[26:27]
	v_pk_fma_f32 v[10:11], v[160:161], v[10:11], v[22:23]
	v_pk_fma_f32 v[8:9], v[162:163], v[8:9], v[28:29]
	v_cvt_pk_bf16_f32 v20, v12, v13
	v_cvt_pk_bf16_f32 v21, v14, v15
	s_nop 0
	v_cvt_pk_bf16_f32 v22, v8, v9
	v_cvt_pk_bf16_f32 v23, v10, v11
	global_store_dwordx4 v[24:25], v[20:23], off
	s_cbranch_vccnz .LBB0_757
	s_nop 0
	v_mov_b32_e32 v20, v173
	v_mov_b32_e32 v21, v173
	v_cvt_pk_fp8_f32 v20, v12, v13
	v_cvt_pk_fp8_f32 v21, v8, v9
	v_readlane_b32 s10, v252, 21
	v_readlane_b32 s11, v252, 22
	v_cvt_pk_fp8_f32 v20, v14, v15 op_sel:[0,0,1]
	v_cvt_pk_fp8_f32 v21, v10, v11 op_sel:[0,0,1]
	v_lshl_add_u64 v[22:23], s[10:11], 0, v[18:19]
	global_store_dwordx2 v[22:23], v[20:21], off
.LBB0_757:
	v_or_b32_e32 v18, 0x80, v18
	v_lshl_add_u64 v[24:25], v[18:19], 1, s[4:5]
	s_nop 0
	s_and_b64 vcc, exec, s[42:43]
	s_waitcnt vmcnt(15)
	v_mov_b32_e32 v20, v244
	v_mov_b32_e32 v21, v245
	v_mov_b32_e32 v22, v246
	v_mov_b32_e32 v23, v247
	v_lshlrev_b32_e32 v26, 16, v20
	v_and_b32_e32 v27, 0xffff0000, v20
	v_lshlrev_b32_e32 v20, 16, v21
	v_and_b32_e32 v21, 0xffff0000, v21
	v_lshlrev_b32_e32 v28, 16, v22
	v_and_b32_e32 v29, 0xffff0000, v22
	v_lshlrev_b32_e32 v22, 16, v23
	v_and_b32_e32 v23, 0xffff0000, v23
	v_pk_fma_f32 v[6:7], v[160:161], v[6:7], v[20:21]
	v_pk_fma_f32 v[4:5], v[162:163], v[4:5], v[26:27]
	v_pk_fma_f32 v[2:3], v[160:161], v[2:3], v[22:23]
	v_pk_fma_f32 v[0:1], v[162:163], v[0:1], v[28:29]
	v_cvt_pk_bf16_f32 v20, v4, v5
	v_cvt_pk_bf16_f32 v21, v6, v7
	s_nop 0
	v_cvt_pk_bf16_f32 v22, v0, v1
	v_cvt_pk_bf16_f32 v23, v2, v3
	global_store_dwordx4 v[24:25], v[20:23], off
	s_cbranch_vccnz .LBB0_759
	s_nop 0
	v_mov_b32_e32 v20, v173
	v_mov_b32_e32 v21, v173
	v_cvt_pk_fp8_f32 v20, v4, v5
	v_cvt_pk_fp8_f32 v21, v0, v1
	v_readlane_b32 s10, v252, 21
	v_readlane_b32 s11, v252, 22
	v_cvt_pk_fp8_f32 v20, v6, v7 op_sel:[0,0,1]
	v_cvt_pk_fp8_f32 v21, v2, v3 op_sel:[0,0,1]
	v_lshl_add_u64 v[18:19], s[10:11], 0, v[18:19]
	global_store_dwordx2 v[18:19], v[20:21], off

.LBB0_785:
	s_nop 15
	s_nop 7
	s_lshl_b32 s12, s11, 8
	s_lshl_b32 s8, s10, 8
	v_add_u32_e32 v2, s12, v182
	s_ashr_i32 s9, s8, 31
	v_ashrrev_i32_e32 v3, 31, v2
	v_mov_b32_e32 v1, s9
	v_or_b32_e32 v0, s8, v164
	v_lshlrev_b64 v[4:5], 11, v[2:3]
	v_lshl_add_u64 v[4:5], v[4:5], 0, v[0:1]
	v_lshl_add_u64 v[18:19], v[4:5], 1, s[4:5]
	global_load_dwordx4 v[6:9], v[18:19], off
	global_load_dwordx4 v[174:177], v[18:19], off offset:256
	v_add_u32_e32 v244, s12, v183
	v_ashrrev_i32_e32 v245, 31, v244
	v_lshlrev_b64 v[244:245], 11, v[244:245]
	v_lshl_add_u64 v[244:245], v[244:245], 0, v[0:1]
	v_lshl_add_u64 v[244:245], v[244:245], 1, s[4:5]
	global_load_dwordx4 v[178:181], v[244:245], off
	global_load_dwordx4 v[200:203], v[244:245], off offset:256
	v_add_u32_e32 v244, s12, v184
	v_ashrrev_i32_e32 v245, 31, v244
	v_lshlrev_b64 v[244:245], 11, v[244:245]
	v_lshl_add_u64 v[244:245], v[244:245], 0, v[0:1]
	v_lshl_add_u64 v[244:245], v[244:245], 1, s[4:5]
	global_load_dwordx4 v[204:207], v[244:245], off
	global_load_dwordx4 v[208:211], v[244:245], off offset:256
	v_add_u32_e32 v244, s12, v185
	v_ashrrev_i32_e32 v245, 31, v244
	v_lshlrev_b64 v[244:245], 11, v[244:245]
	v_lshl_add_u64 v[244:245], v[244:245], 0, v[0:1]
	v_lshl_add_u64 v[244:245], v[244:245], 1, s[4:5]
	global_load_dwordx4 v[212:215], v[244:245], off
	global_load_dwordx4 v[224:227], v[244:245], off offset:256
	v_add_u32_e32 v244, 0x80, v2
	v_ashrrev_i32_e32 v245, 31, v244
	v_lshlrev_b64 v[244:245], 11, v[244:245]
	v_lshl_add_u64 v[244:245], v[244:245], 0, v[0:1]
	v_lshl_add_u64 v[244:245], v[244:245], 1, s[4:5]
	global_load_dwordx4 v[228:231], v[244:245], off
	global_load_dwordx4 v[236:239], v[244:245], off offset:256
	v_add_u32_e32 v244, 0x90, v2
	v_ashrrev_i32_e32 v245, 31, v244
	v_lshlrev_b64 v[244:245], 11, v[244:245]
	v_lshl_add_u64 v[244:245], v[244:245], 0, v[0:1]
	v_lshl_add_u64 v[244:245], v[244:245], 1, s[4:5]
	global_load_dwordx4 v[240:243], v[244:245], off
	v_mov_b32_e32 v161, v160
	v_cndmask_b32_e64 v10, 0, 1, s[16:17]
	v_cmp_ne_u32_e64 s[42:43], 1, v10
	s_andn2_b64 vcc, exec, s[16:17]
	s_mov_b64 s[74:75], s[96:97]
	s_waitcnt vmcnt(10)
	v_lshlrev_b32_e32 v12, 16, v6
	v_and_b32_e32 v13, 0xffff0000, v6
	v_lshlrev_b32_e32 v6, 16, v7
	v_and_b32_e32 v7, 0xffff0000, v7
	v_lshlrev_b32_e32 v14, 16, v8
	v_and_b32_e32 v15, 0xffff0000, v8
	v_lshlrev_b32_e32 v8, 16, v9
	v_and_b32_e32 v9, 0xffff0000, v9
	v_pk_fma_f32 v[10:11], v[160:161], v[158:159], v[6:7]
	v_pk_fma_f32 v[12:13], v[162:163], v[156:157], v[12:13]
	v_pk_fma_f32 v[6:7], v[160:161], v[154:155], v[8:9]
	v_pk_fma_f32 v[8:9], v[162:163], v[152:153], v[14:15]
	v_cvt_pk_bf16_f32 v14, v12, v13
	v_cvt_pk_bf16_f32 v15, v10, v11
	s_nop 0
	v_cvt_pk_bf16_f32 v16, v8, v9
	v_cvt_pk_bf16_f32 v17, v6, v7
	global_store_dwordx4 v[18:19], v[14:17], off
	s_cbranch_vccnz .LBB0_787
	s_nop 0
	v_mov_b32_e32 v14, v173
	v_mov_b32_e32 v15, v173
	v_cvt_pk_fp8_f32 v14, v12, v13
	v_cvt_pk_fp8_f32 v15, v8, v9
	v_readlane_b32 s8, v252, 21
	v_readlane_b32 s9, v252, 22
	v_cvt_pk_fp8_f32 v14, v10, v11 op_sel:[0,0,1]
	v_cvt_pk_fp8_f32 v15, v6, v7 op_sel:[0,0,1]
	v_lshl_add_u64 v[16:17], s[8:9], 0, v[4:5]
	global_store_dwordx2 v[16:17], v[14:15], off
.LBB0_787:
	v_or_b32_e32 v4, 0x80, v4
	v_lshl_add_u64 v[26:27], v[4:5], 1, s[4:5]
	s_nop 0
	s_and_b64 vcc, exec, s[42:43]
	s_waitcnt vmcnt(10)
	v_mov_b32_e32 v14, v174
	v_mov_b32_e32 v15, v175
	v_mov_b32_e32 v16, v176
	v_mov_b32_e32 v17, v177
	v_lshlrev_b32_e32 v18, 16, v14
	v_and_b32_e32 v19, 0xffff0000, v14
	v_lshlrev_b32_e32 v14, 16, v15
	v_and_b32_e32 v15, 0xffff0000, v15
	v_lshlrev_b32_e32 v20, 16, v16
	v_and_b32_e32 v21, 0xffff0000, v16
	v_lshlrev_b32_e32 v16, 16, v17
	v_and_b32_e32 v17, 0xffff0000, v17
	v_pk_fma_f32 v[14:15], v[160:161], v[150:151], v[14:15]
	v_pk_fma_f32 v[18:19], v[162:163], v[148:149], v[18:19]
	v_pk_fma_f32 v[16:17], v[160:161], v[146:147], v[16:17]
	v_pk_fma_f32 v[20:21], v[162:163], v[144:145], v[20:21]
	v_cvt_pk_bf16_f32 v22, v18, v19
	v_cvt_pk_bf16_f32 v23, v14, v15
	s_nop 0
	v_cvt_pk_bf16_f32 v24, v20, v21
	v_cvt_pk_bf16_f32 v25, v16, v17
	global_store_dwordx4 v[26:27], v[22:25], off
	s_cbranch_vccnz .LBB0_789
	s_nop 0
	v_mov_b32_e32 v22, v173
	v_mov_b32_e32 v23, v173
	v_cvt_pk_fp8_f32 v22, v18, v19
	v_cvt_pk_fp8_f32 v23, v20, v21
	v_readlane_b32 s8, v252, 21
	v_readlane_b32 s9, v252, 22
	v_cvt_pk_fp8_f32 v22, v14, v15 op_sel:[0,0,1]
	v_cvt_pk_fp8_f32 v23, v16, v17 op_sel:[0,0,1]
	v_lshl_add_u64 v[4:5], s[8:9], 0, v[4:5]
	global_store_dwordx2 v[4:5], v[22:23], off

.LBB0_791:
	s_or_b64 exec, exec, s[10:11]
	v_add_u32_e32 v4, s12, v183
	s_waitcnt lgkmcnt(0)
	v_ashrrev_i32_e32 v5, 31, v4
	v_lshlrev_b64 v[6:7], 11, v[4:5]
	v_lshl_add_u64 v[6:7], v[6:7], 0, v[0:1]
	v_lshl_add_u64 v[20:21], v[6:7], 1, s[4:5]
	v_add_u32_e32 v244, 0x90, v2
	v_ashrrev_i32_e32 v245, 31, v244
	v_lshlrev_b64 v[244:245], 11, v[244:245]
	v_lshl_add_u64 v[244:245], v[244:245], 0, v[0:1]
	v_lshl_add_u64 v[244:245], v[244:245], 1, s[4:5]
	global_load_dwordx4 v[144:147], v[244:245], off offset:256
	v_add_u32_e32 v244, 0xa0, v2
	v_ashrrev_i32_e32 v245, 31, v244
	v_lshlrev_b64 v[244:245], 11, v[244:245]
	v_lshl_add_u64 v[244:245], v[244:245], 0, v[0:1]
	v_lshl_add_u64 v[244:245], v[244:245], 1, s[4:5]
	global_load_dwordx4 v[148:151], v[244:245], off
	global_load_dwordx4 v[152:155], v[244:245], off offset:256
	v_add_u32_e32 v244, 0xb0, v2
	v_ashrrev_i32_e32 v245, 31, v244
	v_lshlrev_b64 v[244:245], 11, v[244:245]
	v_lshl_add_u64 v[244:245], v[244:245], 0, v[0:1]
	v_lshl_add_u64 v[244:245], v[244:245], 1, s[4:5]
	global_load_dwordx4 v[156:159], v[244:245], off
	v_mov_b32_e32 v161, v160
	s_and_b64 vcc, exec, s[42:43]
	s_waitcnt vmcnt(14)
	v_mov_b32_e32 v8, v178
	v_mov_b32_e32 v9, v179
	v_mov_b32_e32 v10, v180
	v_mov_b32_e32 v11, v181
	v_lshlrev_b32_e32 v12, 16, v8
	v_and_b32_e32 v13, 0xffff0000, v8
	v_lshlrev_b32_e32 v8, 16, v9
	v_and_b32_e32 v9, 0xffff0000, v9
	v_lshlrev_b32_e32 v14, 16, v10
	v_and_b32_e32 v15, 0xffff0000, v10
	v_lshlrev_b32_e32 v10, 16, v11
	v_and_b32_e32 v11, 0xffff0000, v11
	v_pk_fma_f32 v[8:9], v[160:161], v[142:143], v[8:9]
	v_pk_fma_f32 v[12:13], v[162:163], v[140:141], v[12:13]
	v_pk_fma_f32 v[10:11], v[160:161], v[138:139], v[10:11]
	v_pk_fma_f32 v[14:15], v[162:163], v[136:137], v[14:15]
	v_cvt_pk_bf16_f32 v16, v12, v13
	v_cvt_pk_bf16_f32 v17, v8, v9
	s_nop 0
	v_cvt_pk_bf16_f32 v18, v14, v15
	v_cvt_pk_bf16_f32 v19, v10, v11
	global_store_dwordx4 v[20:21], v[16:19], off
	s_cbranch_vccnz .LBB0_793
	s_nop 0
	v_mov_b32_e32 v16, v173
	v_mov_b32_e32 v17, v173
	v_cvt_pk_fp8_f32 v16, v12, v13
	v_cvt_pk_fp8_f32 v17, v14, v15
	v_readlane_b32 s10, v252, 21
	v_readlane_b32 s11, v252, 22
	v_cvt_pk_fp8_f32 v16, v8, v9 op_sel:[0,0,1]
	v_cvt_pk_fp8_f32 v17, v10, v11 op_sel:[0,0,1]
	v_lshl_add_u64 v[18:19], s[10:11], 0, v[6:7]
	global_store_dwordx2 v[18:19], v[16:17], off
.LBB0_793:
	v_or_b32_e32 v6, 0x80, v6
	v_lshl_add_u64 v[30:31], v[6:7], 1, s[4:5]
	s_nop 0
	s_and_b64 vcc, exec, s[42:43]
	s_waitcnt vmcnt(14)
	v_mov_b32_e32 v16, v200
	v_mov_b32_e32 v17, v201
	v_mov_b32_e32 v18, v202
	v_mov_b32_e32 v19, v203
	v_lshlrev_b32_e32 v20, 16, v16
	v_and_b32_e32 v21, 0xffff0000, v16
	v_lshlrev_b32_e32 v16, 16, v17
	v_and_b32_e32 v17, 0xffff0000, v17
	v_lshlrev_b32_e32 v22, 16, v18
	v_and_b32_e32 v23, 0xffff0000, v18
	v_lshlrev_b32_e32 v18, 16, v19
	v_and_b32_e32 v19, 0xffff0000, v19
	v_pk_fma_f32 v[16:17], v[160:161], v[134:135], v[16:17]
	v_pk_fma_f32 v[20:21], v[162:163], v[132:133], v[20:21]
	v_pk_fma_f32 v[18:19], v[160:161], v[130:131], v[18:19]
	v_pk_fma_f32 v[22:23], v[162:163], v[128:129], v[22:23]
	v_cvt_pk_bf16_f32 v26, v20, v21
	v_cvt_pk_bf16_f32 v27, v16, v17
	s_nop 0
	v_cvt_pk_bf16_f32 v28, v22, v23
	v_cvt_pk_bf16_f32 v29, v18, v19
	global_store_dwordx4 v[30:31], v[26:29], off
	s_cbranch_vccnz .LBB0_795
	s_nop 0
	v_mov_b32_e32 v26, v173
	v_mov_b32_e32 v27, v173
	v_cvt_pk_fp8_f32 v26, v20, v21
	v_cvt_pk_fp8_f32 v27, v22, v23
	v_readlane_b32 s10, v252, 21
	v_readlane_b32 s11, v252, 22
	v_cvt_pk_fp8_f32 v26, v16, v17 op_sel:[0,0,1]
	v_cvt_pk_fp8_f32 v27, v18, v19 op_sel:[0,0,1]
	v_lshl_add_u64 v[6:7], s[10:11], 0, v[6:7]
	global_store_dwordx2 v[6:7], v[26:27], off

.LBB0_797:
	s_or_b64 exec, exec, s[10:11]
	v_add_u32_e32 v4, s12, v184
	v_ashrrev_i32_e32 v5, 31, v4
	s_waitcnt lgkmcnt(0)
	v_lshlrev_b64 v[6:7], 11, v[4:5]
	v_lshl_add_u64 v[6:7], v[6:7], 0, v[0:1]
	v_lshl_add_u64 v[20:21], v[6:7], 1, s[4:5]
	v_add_u32_e32 v244, 0xb0, v2
	v_ashrrev_i32_e32 v245, 31, v244
	v_lshlrev_b64 v[244:245], 11, v[244:245]
	v_lshl_add_u64 v[244:245], v[244:245], 0, v[0:1]
	v_lshl_add_u64 v[244:245], v[244:245], 1, s[4:5]
	global_load_dwordx4 v[128:131], v[244:245], off offset:256
	v_mov_b32_e32 v161, v160
	s_and_b64 vcc, exec, s[42:43]
	s_waitcnt vmcnt(15)
	v_mov_b32_e32 v8, v204
	v_mov_b32_e32 v9, v205
	v_mov_b32_e32 v10, v206
	v_mov_b32_e32 v11, v207
	v_lshlrev_b32_e32 v12, 16, v8
	v_and_b32_e32 v13, 0xffff0000, v8
	v_lshlrev_b32_e32 v8, 16, v9
	v_and_b32_e32 v9, 0xffff0000, v9
	v_lshlrev_b32_e32 v14, 16, v10
	v_and_b32_e32 v15, 0xffff0000, v10
	v_lshlrev_b32_e32 v10, 16, v11
	v_and_b32_e32 v11, 0xffff0000, v11
	v_pk_fma_f32 v[8:9], v[160:161], v[126:127], v[8:9]
	v_pk_fma_f32 v[12:13], v[162:163], v[124:125], v[12:13]
	v_pk_fma_f32 v[10:11], v[160:161], v[122:123], v[10:11]
	v_pk_fma_f32 v[14:15], v[162:163], v[120:121], v[14:15]
	v_cvt_pk_bf16_f32 v16, v12, v13
	v_cvt_pk_bf16_f32 v17, v8, v9
	s_nop 0
	v_cvt_pk_bf16_f32 v18, v14, v15
	v_cvt_pk_bf16_f32 v19, v10, v11
	global_store_dwordx4 v[20:21], v[16:19], off
	s_cbranch_vccnz .LBB0_799
	s_nop 0
	v_mov_b32_e32 v16, v173
	v_mov_b32_e32 v17, v173
	v_cvt_pk_fp8_f32 v16, v12, v13
	v_cvt_pk_fp8_f32 v17, v14, v15
	v_readlane_b32 s10, v252, 21
	v_readlane_b32 s11, v252, 22
	v_cvt_pk_fp8_f32 v16, v8, v9 op_sel:[0,0,1]
	v_cvt_pk_fp8_f32 v17, v10, v11 op_sel:[0,0,1]
	v_lshl_add_u64 v[18:19], s[10:11], 0, v[6:7]
	global_store_dwordx2 v[18:19], v[16:17], off
.LBB0_799:
	v_or_b32_e32 v6, 0x80, v6
	v_lshl_add_u64 v[30:31], v[6:7], 1, s[4:5]
	s_nop 0
	s_and_b64 vcc, exec, s[42:43]
	s_waitcnt vmcnt(15)
	v_mov_b32_e32 v16, v208
	v_mov_b32_e32 v17, v209
	v_mov_b32_e32 v18, v210
	v_mov_b32_e32 v19, v211
	v_lshlrev_b32_e32 v20, 16, v16
	v_and_b32_e32 v21, 0xffff0000, v16
	v_lshlrev_b32_e32 v16, 16, v17
	v_and_b32_e32 v17, 0xffff0000, v17
	v_lshlrev_b32_e32 v22, 16, v18
	v_and_b32_e32 v23, 0xffff0000, v18
	v_lshlrev_b32_e32 v18, 16, v19
	v_and_b32_e32 v19, 0xffff0000, v19
	v_pk_fma_f32 v[16:17], v[160:161], v[118:119], v[16:17]
	v_pk_fma_f32 v[20:21], v[162:163], v[116:117], v[20:21]
	v_pk_fma_f32 v[18:19], v[160:161], v[114:115], v[18:19]
	v_pk_fma_f32 v[22:23], v[162:163], v[112:113], v[22:23]
	v_cvt_pk_bf16_f32 v26, v20, v21
	v_cvt_pk_bf16_f32 v27, v16, v17
	s_nop 0
	v_cvt_pk_bf16_f32 v28, v22, v23
	v_cvt_pk_bf16_f32 v29, v18, v19
	global_store_dwordx4 v[30:31], v[26:29], off
	s_cbranch_vccnz .LBB0_801
	s_nop 0
	v_mov_b32_e32 v26, v173
	v_mov_b32_e32 v27, v173
	v_cvt_pk_fp8_f32 v26, v20, v21
	v_cvt_pk_fp8_f32 v27, v22, v23
	v_readlane_b32 s10, v252, 21
	v_readlane_b32 s11, v252, 22
	v_cvt_pk_fp8_f32 v26, v16, v17 op_sel:[0,0,1]
	v_cvt_pk_fp8_f32 v27, v18, v19 op_sel:[0,0,1]
	v_lshl_add_u64 v[6:7], s[10:11], 0, v[6:7]
	global_store_dwordx2 v[6:7], v[26:27], off

.LBB0_803:
	s_or_b64 exec, exec, s[10:11]
	v_add_u32_e32 v4, s12, v185
	v_ashrrev_i32_e32 v5, 31, v4
	s_waitcnt lgkmcnt(0)
	v_lshlrev_b64 v[6:7], 11, v[4:5]
	v_lshl_add_u64 v[6:7], v[6:7], 0, v[0:1]
	v_lshl_add_u64 v[20:21], v[6:7], 1, s[4:5]
	s_nop 0
	v_mov_b32_e32 v161, v160
	s_and_b64 vcc, exec, s[42:43]
	s_waitcnt vmcnt(15)
	v_mov_b32_e32 v8, v212
	v_mov_b32_e32 v9, v213
	v_mov_b32_e32 v10, v214
	v_mov_b32_e32 v11, v215
	v_lshlrev_b32_e32 v12, 16, v8
	v_and_b32_e32 v13, 0xffff0000, v8
	v_lshlrev_b32_e32 v8, 16, v9
	v_and_b32_e32 v9, 0xffff0000, v9
	v_lshlrev_b32_e32 v14, 16, v10
	v_and_b32_e32 v15, 0xffff0000, v10
	v_lshlrev_b32_e32 v10, 16, v11
	v_and_b32_e32 v11, 0xffff0000, v11
	v_pk_fma_f32 v[8:9], v[160:161], v[110:111], v[8:9]
	v_pk_fma_f32 v[12:13], v[162:163], v[108:109], v[12:13]
	v_pk_fma_f32 v[10:11], v[160:161], v[106:107], v[10:11]
	v_pk_fma_f32 v[14:15], v[162:163], v[104:105], v[14:15]
	v_cvt_pk_bf16_f32 v16, v12, v13
	v_cvt_pk_bf16_f32 v17, v8, v9
	s_nop 0
	v_cvt_pk_bf16_f32 v18, v14, v15
	v_cvt_pk_bf16_f32 v19, v10, v11
	global_store_dwordx4 v[20:21], v[16:19], off
	s_cbranch_vccnz .LBB0_805
	s_nop 0
	v_mov_b32_e32 v16, v173
	v_mov_b32_e32 v17, v173
	v_cvt_pk_fp8_f32 v16, v12, v13
	v_cvt_pk_fp8_f32 v17, v14, v15
	v_readlane_b32 s10, v252, 21
	v_readlane_b32 s11, v252, 22
	v_cvt_pk_fp8_f32 v16, v8, v9 op_sel:[0,0,1]
	v_cvt_pk_fp8_f32 v17, v10, v11 op_sel:[0,0,1]
	v_lshl_add_u64 v[18:19], s[10:11], 0, v[6:7]
	global_store_dwordx2 v[18:19], v[16:17], off
.LBB0_805:
	v_or_b32_e32 v6, 0x80, v6
	v_lshl_add_u64 v[30:31], v[6:7], 1, s[4:5]
	s_nop 0
	s_and_b64 vcc, exec, s[42:43]
	s_waitcnt vmcnt(15)
	v_mov_b32_e32 v16, v224
	v_mov_b32_e32 v17, v225
	v_mov_b32_e32 v18, v226
	v_mov_b32_e32 v19, v227
	v_lshlrev_b32_e32 v20, 16, v16
	v_and_b32_e32 v21, 0xffff0000, v16
	v_lshlrev_b32_e32 v16, 16, v17
	v_and_b32_e32 v17, 0xffff0000, v17
	v_lshlrev_b32_e32 v22, 16, v18
	v_and_b32_e32 v23, 0xffff0000, v18
	v_lshlrev_b32_e32 v18, 16, v19
	v_and_b32_e32 v19, 0xffff0000, v19
	v_pk_fma_f32 v[16:17], v[160:161], v[102:103], v[16:17]
	v_pk_fma_f32 v[20:21], v[162:163], v[100:101], v[20:21]
	v_pk_fma_f32 v[18:19], v[160:161], v[98:99], v[18:19]
	v_pk_fma_f32 v[22:23], v[162:163], v[96:97], v[22:23]
	v_cvt_pk_bf16_f32 v26, v20, v21
	v_cvt_pk_bf16_f32 v27, v16, v17
	s_nop 0
	v_cvt_pk_bf16_f32 v28, v22, v23
	v_cvt_pk_bf16_f32 v29, v18, v19
	global_store_dwordx4 v[30:31], v[26:29], off
	s_cbranch_vccnz .LBB0_807
	s_nop 0
	v_mov_b32_e32 v26, v173
	v_mov_b32_e32 v27, v173
	v_cvt_pk_fp8_f32 v26, v20, v21
	v_cvt_pk_fp8_f32 v27, v22, v23
	v_readlane_b32 s10, v252, 21
	v_readlane_b32 s11, v252, 22
	v_cvt_pk_fp8_f32 v26, v16, v17 op_sel:[0,0,1]
	v_cvt_pk_fp8_f32 v27, v18, v19 op_sel:[0,0,1]
	v_lshl_add_u64 v[6:7], s[10:11], 0, v[6:7]
	global_store_dwordx2 v[6:7], v[26:27], off

.LBB0_809:
	s_or_b64 exec, exec, s[10:11]
	v_add_u32_e32 v4, 0x80, v2
	v_ashrrev_i32_e32 v5, 31, v4
	s_waitcnt lgkmcnt(0)
	v_lshlrev_b64 v[6:7], 11, v[4:5]
	v_lshl_add_u64 v[6:7], v[6:7], 0, v[0:1]
	v_lshl_add_u64 v[20:21], v[6:7], 1, s[4:5]
	s_nop 0
	v_mov_b32_e32 v161, v160
	s_and_b64 vcc, exec, s[42:43]
	s_waitcnt vmcnt(15)
	v_mov_b32_e32 v8, v228
	v_mov_b32_e32 v9, v229
	v_mov_b32_e32 v10, v230
	v_mov_b32_e32 v11, v231
	v_lshlrev_b32_e32 v12, 16, v8
	v_and_b32_e32 v13, 0xffff0000, v8
	v_lshlrev_b32_e32 v8, 16, v9
	v_and_b32_e32 v9, 0xffff0000, v9
	v_lshlrev_b32_e32 v14, 16, v10
	v_and_b32_e32 v15, 0xffff0000, v10
	v_lshlrev_b32_e32 v10, 16, v11
	v_and_b32_e32 v11, 0xffff0000, v11
	v_pk_fma_f32 v[8:9], v[160:161], v[94:95], v[8:9]
	v_pk_fma_f32 v[12:13], v[162:163], v[92:93], v[12:13]
	v_pk_fma_f32 v[10:11], v[160:161], v[90:91], v[10:11]
	v_pk_fma_f32 v[14:15], v[162:163], v[88:89], v[14:15]
	v_cvt_pk_bf16_f32 v16, v12, v13
	v_cvt_pk_bf16_f32 v17, v8, v9
	s_nop 0
	v_cvt_pk_bf16_f32 v18, v14, v15
	v_cvt_pk_bf16_f32 v19, v10, v11
	global_store_dwordx4 v[20:21], v[16:19], off
	s_cbranch_vccnz .LBB0_811
	s_nop 0
	v_mov_b32_e32 v16, v173
	v_mov_b32_e32 v17, v173
	v_cvt_pk_fp8_f32 v16, v12, v13
	v_cvt_pk_fp8_f32 v17, v14, v15
	v_readlane_b32 s10, v252, 21
	v_readlane_b32 s11, v252, 22
	v_cvt_pk_fp8_f32 v16, v8, v9 op_sel:[0,0,1]
	v_cvt_pk_fp8_f32 v17, v10, v11 op_sel:[0,0,1]
	v_lshl_add_u64 v[18:19], s[10:11], 0, v[6:7]
	global_store_dwordx2 v[18:19], v[16:17], off
.LBB0_811:
	v_or_b32_e32 v6, 0x80, v6
	v_lshl_add_u64 v[30:31], v[6:7], 1, s[4:5]
	s_nop 0
	s_and_b64 vcc, exec, s[42:43]
	s_waitcnt vmcnt(15)
	v_mov_b32_e32 v16, v236
	v_mov_b32_e32 v17, v237
	v_mov_b32_e32 v18, v238
	v_mov_b32_e32 v19, v239
	v_lshlrev_b32_e32 v20, 16, v16
	v_and_b32_e32 v21, 0xffff0000, v16
	v_lshlrev_b32_e32 v16, 16, v17
	v_and_b32_e32 v17, 0xffff0000, v17
	v_lshlrev_b32_e32 v22, 16, v18
	v_and_b32_e32 v23, 0xffff0000, v18
	v_lshlrev_b32_e32 v18, 16, v19
	v_and_b32_e32 v19, 0xffff0000, v19
	v_pk_fma_f32 v[16:17], v[160:161], v[86:87], v[16:17]
	v_pk_fma_f32 v[20:21], v[162:163], v[84:85], v[20:21]
	v_pk_fma_f32 v[18:19], v[160:161], v[82:83], v[18:19]
	v_pk_fma_f32 v[22:23], v[162:163], v[80:81], v[22:23]
	v_cvt_pk_bf16_f32 v26, v20, v21
	v_cvt_pk_bf16_f32 v27, v16, v17
	s_nop 0
	v_cvt_pk_bf16_f32 v28, v22, v23
	v_cvt_pk_bf16_f32 v29, v18, v19
	global_store_dwordx4 v[30:31], v[26:29], off
	s_cbranch_vccnz .LBB0_813
	s_nop 0
	v_mov_b32_e32 v26, v173
	v_mov_b32_e32 v27, v173
	v_cvt_pk_fp8_f32 v26, v20, v21
	v_cvt_pk_fp8_f32 v27, v22, v23
	v_readlane_b32 s10, v252, 21
	v_readlane_b32 s11, v252, 22
	v_cvt_pk_fp8_f32 v26, v16, v17 op_sel:[0,0,1]
	v_cvt_pk_fp8_f32 v27, v18, v19 op_sel:[0,0,1]
	v_lshl_add_u64 v[6:7], s[10:11], 0, v[6:7]
	global_store_dwordx2 v[6:7], v[26:27], off

.LBB0_815:
	s_or_b64 exec, exec, s[10:11]
	v_add_u32_e32 v4, 0x90, v2
	v_ashrrev_i32_e32 v5, 31, v4
	s_waitcnt lgkmcnt(0)
	v_lshlrev_b64 v[6:7], 11, v[4:5]
	v_lshl_add_u64 v[6:7], v[6:7], 0, v[0:1]
	v_lshl_add_u64 v[20:21], v[6:7], 1, s[4:5]
	s_nop 0
	v_mov_b32_e32 v161, v160
	s_and_b64 vcc, exec, s[42:43]
	s_waitcnt vmcnt(15)
	v_mov_b32_e32 v8, v240
	v_mov_b32_e32 v9, v241
	v_mov_b32_e32 v10, v242
	v_mov_b32_e32 v11, v243
	v_lshlrev_b32_e32 v12, 16, v8
	v_and_b32_e32 v13, 0xffff0000, v8
	v_lshlrev_b32_e32 v8, 16, v9
	v_and_b32_e32 v9, 0xffff0000, v9
	v_lshlrev_b32_e32 v14, 16, v10
	v_and_b32_e32 v15, 0xffff0000, v10
	v_lshlrev_b32_e32 v10, 16, v11
	v_and_b32_e32 v11, 0xffff0000, v11
	v_pk_fma_f32 v[8:9], v[160:161], v[78:79], v[8:9]
	v_pk_fma_f32 v[12:13], v[162:163], v[76:77], v[12:13]
	v_pk_fma_f32 v[10:11], v[160:161], v[74:75], v[10:11]
	v_pk_fma_f32 v[14:15], v[162:163], v[72:73], v[14:15]
	v_cvt_pk_bf16_f32 v16, v12, v13
	v_cvt_pk_bf16_f32 v17, v8, v9
	s_nop 0
	v_cvt_pk_bf16_f32 v18, v14, v15
	v_cvt_pk_bf16_f32 v19, v10, v11
	global_store_dwordx4 v[20:21], v[16:19], off
	s_cbranch_vccnz .LBB0_817
	s_nop 0
	v_mov_b32_e32 v16, v173
	v_mov_b32_e32 v17, v173
	v_cvt_pk_fp8_f32 v16, v12, v13
	v_cvt_pk_fp8_f32 v17, v14, v15
	v_readlane_b32 s10, v252, 21
	v_readlane_b32 s11, v252, 22
	v_cvt_pk_fp8_f32 v16, v8, v9 op_sel:[0,0,1]
	v_cvt_pk_fp8_f32 v17, v10, v11 op_sel:[0,0,1]
	v_lshl_add_u64 v[18:19], s[10:11], 0, v[6:7]
	global_store_dwordx2 v[18:19], v[16:17], off
.LBB0_817:
	v_or_b32_e32 v6, 0x80, v6
	v_lshl_add_u64 v[30:31], v[6:7], 1, s[4:5]
	s_nop 0
	s_and_b64 vcc, exec, s[42:43]
	s_waitcnt vmcnt(13)
	v_mov_b32_e32 v16, v144
	v_mov_b32_e32 v17, v145
	v_mov_b32_e32 v18, v146
	v_mov_b32_e32 v19, v147
	v_lshlrev_b32_e32 v20, 16, v16
	v_and_b32_e32 v21, 0xffff0000, v16
	v_lshlrev_b32_e32 v16, 16, v17
	v_and_b32_e32 v17, 0xffff0000, v17
	v_lshlrev_b32_e32 v22, 16, v18
	v_and_b32_e32 v23, 0xffff0000, v18
	v_lshlrev_b32_e32 v18, 16, v19
	v_and_b32_e32 v19, 0xffff0000, v19
	v_pk_fma_f32 v[16:17], v[160:161], v[70:71], v[16:17]
	v_pk_fma_f32 v[20:21], v[162:163], v[68:69], v[20:21]
	v_pk_fma_f32 v[18:19], v[160:161], v[66:67], v[18:19]
	v_pk_fma_f32 v[22:23], v[162:163], v[64:65], v[22:23]
	v_cvt_pk_bf16_f32 v26, v20, v21
	v_cvt_pk_bf16_f32 v27, v16, v17
	s_nop 0
	v_cvt_pk_bf16_f32 v28, v22, v23
	v_cvt_pk_bf16_f32 v29, v18, v19
	global_store_dwordx4 v[30:31], v[26:29], off
	s_cbranch_vccnz .LBB0_819
	s_nop 0
	v_mov_b32_e32 v26, v173
	v_mov_b32_e32 v27, v173
	v_cvt_pk_fp8_f32 v26, v20, v21
	v_cvt_pk_fp8_f32 v27, v22, v23
	v_readlane_b32 s10, v252, 21
	v_readlane_b32 s11, v252, 22
	v_cvt_pk_fp8_f32 v26, v16, v17 op_sel:[0,0,1]
	v_cvt_pk_fp8_f32 v27, v18, v19 op_sel:[0,0,1]
	v_lshl_add_u64 v[6:7], s[10:11], 0, v[6:7]
	global_store_dwordx2 v[6:7], v[26:27], off

.LBB0_821:
	s_or_b64 exec, exec, s[10:11]
	v_add_u32_e32 v4, 0xa0, v2
	v_ashrrev_i32_e32 v5, 31, v4
	s_waitcnt lgkmcnt(0)
	v_lshlrev_b64 v[6:7], 11, v[4:5]
	v_lshl_add_u64 v[6:7], v[6:7], 0, v[0:1]
	v_lshl_add_u64 v[20:21], v[6:7], 1, s[4:5]
	s_nop 0
	v_mov_b32_e32 v161, v160
	s_and_b64 vcc, exec, s[42:43]
	s_waitcnt vmcnt(13)
	v_mov_b32_e32 v8, v148
	v_mov_b32_e32 v9, v149
	v_mov_b32_e32 v10, v150
	v_mov_b32_e32 v11, v151
	v_lshlrev_b32_e32 v12, 16, v8
	v_and_b32_e32 v13, 0xffff0000, v8
	v_lshlrev_b32_e32 v8, 16, v9
	v_and_b32_e32 v9, 0xffff0000, v9
	v_lshlrev_b32_e32 v14, 16, v10
	v_and_b32_e32 v15, 0xffff0000, v10
	v_lshlrev_b32_e32 v10, 16, v11
	v_and_b32_e32 v11, 0xffff0000, v11
	v_pk_fma_f32 v[8:9], v[160:161], v[62:63], v[8:9]
	v_pk_fma_f32 v[12:13], v[162:163], v[60:61], v[12:13]
	v_pk_fma_f32 v[10:11], v[160:161], v[58:59], v[10:11]
	v_pk_fma_f32 v[14:15], v[162:163], v[56:57], v[14:15]
	v_cvt_pk_bf16_f32 v16, v12, v13
	v_cvt_pk_bf16_f32 v17, v8, v9
	s_nop 0
	v_cvt_pk_bf16_f32 v18, v14, v15
	v_cvt_pk_bf16_f32 v19, v10, v11
	global_store_dwordx4 v[20:21], v[16:19], off
	s_cbranch_vccnz .LBB0_823
	s_nop 0
	v_mov_b32_e32 v16, v173
	v_mov_b32_e32 v17, v173
	v_cvt_pk_fp8_f32 v16, v12, v13
	v_cvt_pk_fp8_f32 v17, v14, v15
	v_readlane_b32 s10, v252, 21
	v_readlane_b32 s11, v252, 22
	v_cvt_pk_fp8_f32 v16, v8, v9 op_sel:[0,0,1]
	v_cvt_pk_fp8_f32 v17, v10, v11 op_sel:[0,0,1]
	v_lshl_add_u64 v[18:19], s[10:11], 0, v[6:7]
	global_store_dwordx2 v[18:19], v[16:17], off
.LBB0_823:
	v_or_b32_e32 v6, 0x80, v6
	v_lshl_add_u64 v[30:31], v[6:7], 1, s[4:5]
	s_nop 0
	s_and_b64 vcc, exec, s[42:43]
	s_waitcnt vmcnt(13)
	v_mov_b32_e32 v16, v152
	v_mov_b32_e32 v17, v153
	v_mov_b32_e32 v18, v154
	v_mov_b32_e32 v19, v155
	v_lshlrev_b32_e32 v20, 16, v16
	v_and_b32_e32 v21, 0xffff0000, v16
	v_lshlrev_b32_e32 v16, 16, v17
	v_and_b32_e32 v17, 0xffff0000, v17
	v_lshlrev_b32_e32 v22, 16, v18
	v_and_b32_e32 v23, 0xffff0000, v18
	v_lshlrev_b32_e32 v18, 16, v19
	v_and_b32_e32 v19, 0xffff0000, v19
	v_pk_fma_f32 v[16:17], v[160:161], v[54:55], v[16:17]
	v_pk_fma_f32 v[20:21], v[162:163], v[52:53], v[20:21]
	v_pk_fma_f32 v[18:19], v[160:161], v[50:51], v[18:19]
	v_pk_fma_f32 v[22:23], v[162:163], v[48:49], v[22:23]
	v_cvt_pk_bf16_f32 v26, v20, v21
	v_cvt_pk_bf16_f32 v27, v16, v17
	s_nop 0
	v_cvt_pk_bf16_f32 v28, v22, v23
	v_cvt_pk_bf16_f32 v29, v18, v19
	global_store_dwordx4 v[30:31], v[26:29], off
	s_cbranch_vccnz .LBB0_825
	s_nop 0
	v_mov_b32_e32 v26, v173
	v_mov_b32_e32 v27, v173
	v_cvt_pk_fp8_f32 v26, v20, v21
	v_cvt_pk_fp8_f32 v27, v22, v23
	v_readlane_b32 s10, v252, 21
	v_readlane_b32 s11, v252, 22
	v_cvt_pk_fp8_f32 v26, v16, v17 op_sel:[0,0,1]
	v_cvt_pk_fp8_f32 v27, v18, v19 op_sel:[0,0,1]
	v_lshl_add_u64 v[6:7], s[10:11], 0, v[6:7]
	global_store_dwordx2 v[6:7], v[26:27], off

.LBB0_827:
	s_or_b64 exec, exec, s[10:11]
	v_add_u32_e32 v2, 0xb0, v2
	v_ashrrev_i32_e32 v3, 31, v2
	v_lshlrev_b64 v[4:5], 11, v[2:3]
	v_lshl_add_u64 v[0:1], v[4:5], 0, v[0:1]
	v_lshl_add_u64 v[16:17], v[0:1], 1, s[4:5]
	s_waitcnt lgkmcnt(0)
	s_nop 0
	v_mov_b32_e32 v161, v160
	s_and_b64 vcc, exec, s[42:43]
	s_waitcnt vmcnt(13)
	v_mov_b32_e32 v4, v156
	v_mov_b32_e32 v5, v157
	v_mov_b32_e32 v6, v158
	v_mov_b32_e32 v7, v159
	v_lshlrev_b32_e32 v8, 16, v4
	v_and_b32_e32 v9, 0xffff0000, v4
	v_lshlrev_b32_e32 v4, 16, v5
	v_and_b32_e32 v5, 0xffff0000, v5
	v_lshlrev_b32_e32 v10, 16, v6
	v_and_b32_e32 v11, 0xffff0000, v6
	v_lshlrev_b32_e32 v6, 16, v7
	v_and_b32_e32 v7, 0xffff0000, v7
	v_pk_fma_f32 v[4:5], v[160:161], v[46:47], v[4:5]
	v_pk_fma_f32 v[8:9], v[162:163], v[44:45], v[8:9]
	v_pk_fma_f32 v[6:7], v[160:161], v[42:43], v[6:7]
	v_pk_fma_f32 v[10:11], v[162:163], v[40:41], v[10:11]
	v_cvt_pk_bf16_f32 v12, v8, v9
	v_cvt_pk_bf16_f32 v13, v4, v5
	s_nop 0
	v_cvt_pk_bf16_f32 v14, v10, v11
	v_cvt_pk_bf16_f32 v15, v6, v7
	global_store_dwordx4 v[16:17], v[12:15], off
	s_cbranch_vccnz .LBB0_829
	s_nop 0
	v_mov_b32_e32 v12, v173
	v_mov_b32_e32 v13, v173
	v_cvt_pk_fp8_f32 v12, v8, v9
	v_cvt_pk_fp8_f32 v13, v10, v11
	v_readlane_b32 s10, v252, 21
	v_readlane_b32 s11, v252, 22
	v_cvt_pk_fp8_f32 v12, v4, v5 op_sel:[0,0,1]
	v_cvt_pk_fp8_f32 v13, v6, v7 op_sel:[0,0,1]
	v_lshl_add_u64 v[14:15], s[10:11], 0, v[0:1]
	global_store_dwordx2 v[14:15], v[12:13], off
.LBB0_829:
	v_or_b32_e32 v0, 0x80, v0
	v_lshl_add_u64 v[26:27], v[0:1], 1, s[4:5]
	s_nop 0
	s_and_b64 vcc, exec, s[42:43]
	s_waitcnt vmcnt(11)
	v_mov_b32_e32 v12, v128
	v_mov_b32_e32 v13, v129
	v_mov_b32_e32 v14, v130
	v_mov_b32_e32 v15, v131
	v_lshlrev_b32_e32 v16, 16, v12
	v_and_b32_e32 v17, 0xffff0000, v12
	v_lshlrev_b32_e32 v12, 16, v13
	v_and_b32_e32 v13, 0xffff0000, v13
	v_lshlrev_b32_e32 v18, 16, v14
	v_and_b32_e32 v19, 0xffff0000, v14
	v_lshlrev_b32_e32 v14, 16, v15
	v_and_b32_e32 v15, 0xffff0000, v15
	v_pk_fma_f32 v[12:13], v[160:161], v[38:39], v[12:13]
	v_pk_fma_f32 v[16:17], v[162:163], v[36:37], v[16:17]
	v_pk_fma_f32 v[14:15], v[160:161], v[34:35], v[14:15]
	v_pk_fma_f32 v[18:19], v[162:163], v[32:33], v[18:19]
	v_cvt_pk_bf16_f32 v20, v16, v17
	v_cvt_pk_bf16_f32 v21, v12, v13
	s_nop 0
	v_cvt_pk_bf16_f32 v22, v18, v19
	v_cvt_pk_bf16_f32 v23, v14, v15
	global_store_dwordx4 v[26:27], v[20:23], off
	s_cbranch_vccnz .LBB0_831
	s_nop 0
	v_mov_b32_e32 v20, v173
	v_mov_b32_e32 v21, v173
	v_cvt_pk_fp8_f32 v20, v16, v17
	v_cvt_pk_fp8_f32 v21, v18, v19
	v_readlane_b32 s10, v252, 21
	v_readlane_b32 s11, v252, 22
	v_cvt_pk_fp8_f32 v20, v12, v13 op_sel:[0,0,1]
	v_cvt_pk_fp8_f32 v21, v14, v15 op_sel:[0,0,1]
	v_lshl_add_u64 v[0:1], s[10:11], 0, v[0:1]
	global_store_dwordx2 v[0:1], v[20:21], off

.LBB0_1161:
	s_nop 15
	s_nop 7
	s_lshl_b32 s12, s10, 8
	v_add_u32_e32 v2, s12, v165
	s_lshl_b32 s8, s11, 8
	v_ashrrev_i32_e32 v3, 31, v2
	s_ashr_i32 s9, s8, 31
	v_lshlrev_b64 v[4:5], 12, v[2:3]
	v_mov_b32_e32 v1, s9
	v_or_b32_e32 v0, s8, v164
	v_lshl_add_u64 v[4:5], s[4:5], 0, v[4:5]
	v_lshl_add_u64 v[8:9], v[0:1], 1, v[4:5]
	global_load_dwordx4 v[4:7], v[8:9], off
	global_load_dwordx4 v[28:31], v[8:9], off offset:256
	v_add_u32_e32 v26, s12, v166
	v_ashrrev_i32_e32 v27, 31, v26
	v_lshlrev_b64 v[26:27], 12, v[26:27]
	v_lshl_add_u64 v[26:27], s[4:5], 0, v[26:27]
	v_lshl_add_u64 v[26:27], v[0:1], 1, v[26:27]
	global_load_dwordx4 v[174:177], v[26:27], off
	global_load_dwordx4 v[178:181], v[26:27], off offset:256
	v_add_u32_e32 v26, s12, v167
	v_ashrrev_i32_e32 v27, 31, v26
	v_lshlrev_b64 v[26:27], 12, v[26:27]
	v_lshl_add_u64 v[26:27], s[4:5], 0, v[26:27]
	v_lshl_add_u64 v[26:27], v[0:1], 1, v[26:27]
	global_load_dwordx4 v[198:201], v[26:27], off
	global_load_dwordx4 v[202:205], v[26:27], off offset:256
	v_add_u32_e32 v26, s12, v172
	v_ashrrev_i32_e32 v27, 31, v26
	v_lshlrev_b64 v[26:27], 12, v[26:27]
	v_lshl_add_u64 v[26:27], s[4:5], 0, v[26:27]
	v_lshl_add_u64 v[26:27], v[0:1], 1, v[26:27]
	global_load_dwordx4 v[206:209], v[26:27], off
	global_load_dwordx4 v[210:213], v[26:27], off offset:256
	v_add_u32_e32 v26, 0x80, v2
	v_ashrrev_i32_e32 v27, 31, v26
	v_lshlrev_b64 v[26:27], 12, v[26:27]
	v_lshl_add_u64 v[26:27], s[4:5], 0, v[26:27]
	v_lshl_add_u64 v[26:27], v[0:1], 1, v[26:27]
	global_load_dwordx4 v[224:227], v[26:27], off
	global_load_dwordx4 v[228:231], v[26:27], off offset:256
	v_add_u32_e32 v26, 0x90, v2
	v_ashrrev_i32_e32 v27, 31, v26
	v_lshlrev_b64 v[26:27], 12, v[26:27]
	v_lshl_add_u64 v[26:27], s[4:5], 0, v[26:27]
	v_lshl_add_u64 v[26:27], v[0:1], 1, v[26:27]
	global_load_dwordx4 v[236:239], v[26:27], off
	global_load_dwordx4 v[240:243], v[26:27], off offset:256
	v_add_u32_e32 v26, 0xa0, v2
	v_ashrrev_i32_e32 v27, 31, v26
	v_lshlrev_b64 v[26:27], 12, v[26:27]
	v_lshl_add_u64 v[26:27], s[4:5], 0, v[26:27]
	v_lshl_add_u64 v[26:27], v[0:1], 1, v[26:27]
	global_load_dwordx4 v[244:247], v[26:27], off
	s_mov_b32 s10, 0x3d000000
	s_lshl_b32 s8, s11, 2
	s_ashr_i32 s9, s8, 31
	s_waitcnt vmcnt(12)
	v_lshlrev_b32_e32 v10, 16, v4
	v_and_b32_e32 v11, 0xffff0000, v4
	v_lshlrev_b32_e32 v4, 16, v5
	v_and_b32_e32 v5, 0xffff0000, v5
	v_lshlrev_b32_e32 v12, 16, v6
	v_and_b32_e32 v13, 0xffff0000, v6
	v_lshlrev_b32_e32 v6, 16, v7
	v_and_b32_e32 v7, 0xffff0000, v7
	v_pk_fma_f32 v[14:15], v[158:159], s[10:11], v[4:5] op_sel_hi:[1,0,1]
	v_pk_fma_f32 v[10:11], v[156:157], s[10:11], v[10:11] op_sel_hi:[1,0,1]
	v_pk_fma_f32 v[16:17], v[154:155], s[10:11], v[6:7] op_sel_hi:[1,0,1]
	v_cvt_pk_bf16_f32 v4, v10, v11
	v_cvt_pk_bf16_f32 v5, v14, v15
	v_pk_fma_f32 v[12:13], v[152:153], s[10:11], v[12:13] op_sel_hi:[1,0,1]
	s_nop 0
	v_cvt_pk_bf16_f32 v6, v12, v13
	v_cvt_pk_bf16_f32 v7, v16, v17
	global_store_dwordx4 v[8:9], v[4:7], off
	s_nop 1
	v_mul_f32_e32 v4, v11, v11
	v_mul_f32_e32 v5, v15, v15
	v_fmac_f32_e32 v4, v10, v10
	v_fmac_f32_e32 v5, v14, v14
	v_add_f32_e32 v4, v4, v5
	v_mul_f32_e32 v5, v13, v13
	v_fmac_f32_e32 v5, v12, v12
	v_add_f32_e32 v4, v5, v4
	v_mul_f32_e32 v5, v17, v17
	v_fmac_f32_e32 v5, v16, v16
	v_add_f32_e32 v18, v5, v4
	s_nop 0
	s_waitcnt vmcnt(12)
	v_mov_b32_e32 v4, v28
	v_mov_b32_e32 v5, v29
	v_mov_b32_e32 v6, v30
	v_mov_b32_e32 v7, v31
	v_lshlrev_b32_e32 v10, 16, v4
	v_and_b32_e32 v11, 0xffff0000, v4
	v_lshlrev_b32_e32 v4, 16, v5
	v_and_b32_e32 v5, 0xffff0000, v5
	v_lshlrev_b32_e32 v12, 16, v6
	v_and_b32_e32 v13, 0xffff0000, v6
	v_lshlrev_b32_e32 v6, 16, v7
	v_and_b32_e32 v7, 0xffff0000, v7
	v_pk_fma_f32 v[14:15], v[150:151], s[10:11], v[4:5] op_sel_hi:[1,0,1]
	v_pk_fma_f32 v[10:11], v[148:149], s[10:11], v[10:11] op_sel_hi:[1,0,1]
	v_pk_fma_f32 v[16:17], v[146:147], s[10:11], v[6:7] op_sel_hi:[1,0,1]
	v_cvt_pk_bf16_f32 v4, v10, v11
	v_cvt_pk_bf16_f32 v5, v14, v15
	v_pk_fma_f32 v[12:13], v[144:145], s[10:11], v[12:13] op_sel_hi:[1,0,1]
	s_nop 0
	v_cvt_pk_bf16_f32 v6, v12, v13
	v_cvt_pk_bf16_f32 v7, v16, v17
	global_store_dwordx4 v[8:9], v[4:7], off offset:256
	s_nop 1
	v_mul_f32_e32 v4, v11, v11
	v_mul_f32_e32 v5, v15, v15
	v_fmac_f32_e32 v4, v10, v10
	v_fmac_f32_e32 v5, v14, v14
	v_add_f32_e32 v4, v4, v5
	v_mul_f32_e32 v5, v13, v13
	v_fmac_f32_e32 v5, v12, v12
	v_add_f32_e32 v4, v5, v4
	v_mul_f32_e32 v5, v17, v17
	v_fmac_f32_e32 v5, v16, v16
	v_and_b32_e32 v6, 64, v188
	v_add_f32_e32 v4, v5, v4
	v_xor_b32_e32 v5, 16, v188
	v_add_u32_e32 v7, 64, v6
	v_cmp_lt_i32_e32 vcc, v5, v7
	v_add_f32_e32 v4, v18, v4
	s_nop 0
	v_cndmask_b32_e32 v5, v188, v5, vcc
	v_lshlrev_b32_e32 v6, 2, v5
	ds_bpermute_b32 v5, v6, v4
	s_waitcnt lgkmcnt(0)
	v_add_f32_e32 v4, v4, v5
	v_xor_b32_e32 v5, 32, v188
	v_cmp_lt_i32_e32 vcc, v5, v7
	s_nop 1
	v_cndmask_b32_e32 v5, v188, v5, vcc
	v_lshlrev_b32_e32 v7, 2, v5
	ds_bpermute_b32 v5, v7, v4
	s_and_saveexec_b64 s[10:11], s[38:39]
	s_mov_b64 s[74:75], s[96:97]
	s_cbranch_execz .LBB0_1163
	v_lshlrev_b64 v[8:9], 7, v[2:3]
	v_lshl_add_u64 v[8:9], s[50:51], 0, v[8:9]
	v_lshl_add_u64 v[8:9], s[8:9], 2, v[8:9]
	s_lshl_b32 s14, s17, 2
	s_mov_b32 s15, s60
	v_lshl_add_u64 v[8:9], v[8:9], 0, s[14:15]
	s_waitcnt lgkmcnt(0)
	v_add_f32_e32 v3, v4, v5
	global_store_dword v[8:9], v3, off
.LBB0_1163:
	s_or_b64 exec, exec, s[10:11]
	v_add_u32_e32 v4, s12, v166
	s_waitcnt lgkmcnt(0)
	v_ashrrev_i32_e32 v5, 31, v4
	v_lshlrev_b64 v[8:9], 12, v[4:5]
	v_lshl_add_u64 v[8:9], s[4:5], 0, v[8:9]
	v_lshl_add_u64 v[16:17], v[0:1], 1, v[8:9]
	v_add_u32_e32 v26, 0xa0, v2
	v_ashrrev_i32_e32 v27, 31, v26
	v_lshlrev_b64 v[26:27], 12, v[26:27]
	v_lshl_add_u64 v[26:27], s[4:5], 0, v[26:27]
	v_lshl_add_u64 v[26:27], v[0:1], 1, v[26:27]
	global_load_dwordx4 v[144:147], v[26:27], off offset:256
	v_add_u32_e32 v26, 0xb0, v2
	v_ashrrev_i32_e32 v27, 31, v26
	v_lshlrev_b64 v[26:27], 12, v[26:27]
	v_lshl_add_u64 v[26:27], s[4:5], 0, v[26:27]
	v_lshl_add_u64 v[26:27], v[0:1], 1, v[26:27]
	global_load_dwordx4 v[148:151], v[26:27], off
	global_load_dwordx4 v[152:155], v[26:27], off offset:256
	s_mov_b32 s10, 0x3d000000
	s_waitcnt vmcnt(15)
	v_mov_b32_e32 v8, v174
	v_mov_b32_e32 v9, v175
	v_mov_b32_e32 v10, v176
	v_mov_b32_e32 v11, v177
	v_lshlrev_b32_e32 v12, 16, v8
	v_and_b32_e32 v13, 0xffff0000, v8
	v_lshlrev_b32_e32 v8, 16, v9
	v_and_b32_e32 v9, 0xffff0000, v9
	v_lshlrev_b32_e32 v14, 16, v10
	v_and_b32_e32 v15, 0xffff0000, v10
	v_lshlrev_b32_e32 v10, 16, v11
	v_and_b32_e32 v11, 0xffff0000, v11
	v_pk_fma_f32 v[18:19], v[142:143], s[10:11], v[8:9] op_sel_hi:[1,0,1]
	v_pk_fma_f32 v[20:21], v[140:141], s[10:11], v[12:13] op_sel_hi:[1,0,1]
	v_pk_fma_f32 v[22:23], v[138:139], s[10:11], v[10:11] op_sel_hi:[1,0,1]
	v_pk_fma_f32 v[24:25], v[136:137], s[10:11], v[14:15] op_sel_hi:[1,0,1]
	v_cvt_pk_bf16_f32 v8, v20, v21
	v_cvt_pk_bf16_f32 v9, v18, v19
	v_mul_f32_e32 v3, v21, v21
	v_cvt_pk_bf16_f32 v10, v24, v25
	v_cvt_pk_bf16_f32 v11, v22, v23
	s_nop 0
	v_mul_f32_e32 v19, v19, v19
	v_mul_f32_e32 v21, v25, v25
	v_fmac_f32_e32 v3, v20, v20
	v_fmac_f32_e32 v19, v18, v18
	v_mul_f32_e32 v23, v23, v23
	v_fmac_f32_e32 v21, v24, v24
	v_add_f32_e32 v3, v3, v19
	v_fmac_f32_e32 v23, v22, v22
	v_add_f32_e32 v3, v21, v3
	v_add_f32_e32 v3, v23, v3
	global_store_dwordx4 v[16:17], v[8:11], off
	s_waitcnt vmcnt(15)
	v_mov_b32_e32 v12, v178
	v_mov_b32_e32 v13, v179
	v_mov_b32_e32 v14, v180
	v_mov_b32_e32 v15, v181
	v_lshlrev_b32_e32 v18, 16, v12
	v_and_b32_e32 v19, 0xffff0000, v12
	v_lshlrev_b32_e32 v12, 16, v13
	v_and_b32_e32 v13, 0xffff0000, v13
	v_lshlrev_b32_e32 v20, 16, v14
	v_and_b32_e32 v21, 0xffff0000, v14
	v_pk_fma_f32 v[12:13], v[134:135], s[10:11], v[12:13] op_sel_hi:[1,0,1]
	v_pk_fma_f32 v[18:19], v[132:133], s[10:11], v[18:19] op_sel_hi:[1,0,1]
	v_lshlrev_b32_e32 v14, 16, v15
	v_and_b32_e32 v15, 0xffff0000, v15
	v_pk_fma_f32 v[20:21], v[128:129], s[10:11], v[20:21] op_sel_hi:[1,0,1]
	v_mul_f32_e32 v22, v19, v19
	v_mul_f32_e32 v23, v13, v13
	v_pk_fma_f32 v[14:15], v[130:131], s[10:11], v[14:15] op_sel_hi:[1,0,1]
	v_mul_f32_e32 v24, v21, v21
	v_fmac_f32_e32 v22, v18, v18
	v_fmac_f32_e32 v23, v12, v12
	v_mul_f32_e32 v25, v15, v15
	v_fmac_f32_e32 v24, v20, v20
	v_add_f32_e32 v22, v22, v23
	v_add_f32_e32 v22, v24, v22
	v_fmac_f32_e32 v25, v14, v14
	v_add_f32_e32 v22, v25, v22
	v_add_f32_e32 v3, v3, v22
	ds_bpermute_b32 v22, v6, v3
	v_cvt_pk_bf16_f32 v10, v18, v19
	v_cvt_pk_bf16_f32 v11, v12, v13
	v_cvt_pk_bf16_f32 v12, v20, v21
	v_cvt_pk_bf16_f32 v13, v14, v15
	s_waitcnt lgkmcnt(0)
	v_add_f32_e32 v3, v3, v22
	ds_bpermute_b32 v8, v7, v3
	global_store_dwordx4 v[16:17], v[10:13], off offset:256
	s_and_saveexec_b64 s[10:11], s[38:39]
	s_cbranch_execz .LBB0_1165
	v_lshlrev_b64 v[4:5], 7, v[4:5]
	v_lshl_add_u64 v[4:5], s[50:51], 0, v[4:5]
	v_lshl_add_u64 v[4:5], s[8:9], 2, v[4:5]
	s_lshl_b32 s14, s17, 2
	s_mov_b32 s15, s60
	v_lshl_add_u64 v[4:5], v[4:5], 0, s[14:15]
	s_waitcnt lgkmcnt(0)
	v_add_f32_e32 v3, v3, v8
	global_store_dword v[4:5], v3, off
.LBB0_1165:
	s_or_b64 exec, exec, s[10:11]
	v_add_u32_e32 v4, s12, v167
	v_ashrrev_i32_e32 v5, 31, v4
	s_waitcnt lgkmcnt(0)
	v_lshlrev_b64 v[8:9], 12, v[4:5]
	v_lshl_add_u64 v[8:9], s[4:5], 0, v[8:9]
	v_lshl_add_u64 v[16:17], v[0:1], 1, v[8:9]
	s_nop 0
	s_mov_b32 s10, 0x3d000000
	s_waitcnt vmcnt(15)
	v_mov_b32_e32 v8, v198
	v_mov_b32_e32 v9, v199
	v_mov_b32_e32 v10, v200
	v_mov_b32_e32 v11, v201
	v_lshlrev_b32_e32 v12, 16, v8
	v_and_b32_e32 v13, 0xffff0000, v8
	v_lshlrev_b32_e32 v8, 16, v9
	v_and_b32_e32 v9, 0xffff0000, v9
	v_lshlrev_b32_e32 v14, 16, v10
	v_and_b32_e32 v15, 0xffff0000, v10
	v_lshlrev_b32_e32 v10, 16, v11
	v_and_b32_e32 v11, 0xffff0000, v11
	v_pk_fma_f32 v[18:19], v[126:127], s[10:11], v[8:9] op_sel_hi:[1,0,1]
	v_pk_fma_f32 v[20:21], v[124:125], s[10:11], v[12:13] op_sel_hi:[1,0,1]
	v_pk_fma_f32 v[22:23], v[122:123], s[10:11], v[10:11] op_sel_hi:[1,0,1]
	v_pk_fma_f32 v[24:25], v[120:121], s[10:11], v[14:15] op_sel_hi:[1,0,1]
	v_cvt_pk_bf16_f32 v8, v20, v21
	v_cvt_pk_bf16_f32 v9, v18, v19
	v_mul_f32_e32 v3, v21, v21
	v_cvt_pk_bf16_f32 v10, v24, v25
	v_cvt_pk_bf16_f32 v11, v22, v23
	s_nop 0
	v_mul_f32_e32 v19, v19, v19
	v_mul_f32_e32 v21, v25, v25
	v_fmac_f32_e32 v3, v20, v20
	v_fmac_f32_e32 v19, v18, v18
	v_mul_f32_e32 v23, v23, v23
	v_fmac_f32_e32 v21, v24, v24
	v_add_f32_e32 v3, v3, v19
	v_fmac_f32_e32 v23, v22, v22
	v_add_f32_e32 v3, v21, v3
	v_add_f32_e32 v3, v23, v3
	global_store_dwordx4 v[16:17], v[8:11], off
	s_waitcnt vmcnt(15)
	v_mov_b32_e32 v12, v202
	v_mov_b32_e32 v13, v203
	v_mov_b32_e32 v14, v204
	v_mov_b32_e32 v15, v205
	v_lshlrev_b32_e32 v18, 16, v12
	v_and_b32_e32 v19, 0xffff0000, v12
	v_lshlrev_b32_e32 v12, 16, v13
	v_and_b32_e32 v13, 0xffff0000, v13
	v_lshlrev_b32_e32 v20, 16, v14
	v_and_b32_e32 v21, 0xffff0000, v14
	v_pk_fma_f32 v[12:13], v[118:119], s[10:11], v[12:13] op_sel_hi:[1,0,1]
	v_pk_fma_f32 v[18:19], v[116:117], s[10:11], v[18:19] op_sel_hi:[1,0,1]
	v_lshlrev_b32_e32 v14, 16, v15
	v_and_b32_e32 v15, 0xffff0000, v15
	v_pk_fma_f32 v[20:21], v[112:113], s[10:11], v[20:21] op_sel_hi:[1,0,1]
	v_mul_f32_e32 v22, v19, v19
	v_mul_f32_e32 v23, v13, v13
	v_pk_fma_f32 v[14:15], v[114:115], s[10:11], v[14:15] op_sel_hi:[1,0,1]
	v_mul_f32_e32 v24, v21, v21
	v_fmac_f32_e32 v22, v18, v18
	v_fmac_f32_e32 v23, v12, v12
	v_mul_f32_e32 v25, v15, v15
	v_fmac_f32_e32 v24, v20, v20
	v_add_f32_e32 v22, v22, v23
	v_add_f32_e32 v22, v24, v22
	v_fmac_f32_e32 v25, v14, v14
	v_add_f32_e32 v22, v25, v22
	v_add_f32_e32 v3, v3, v22
	ds_bpermute_b32 v22, v6, v3
	v_cvt_pk_bf16_f32 v10, v18, v19
	v_cvt_pk_bf16_f32 v11, v12, v13
	v_cvt_pk_bf16_f32 v12, v20, v21
	v_cvt_pk_bf16_f32 v13, v14, v15
	s_waitcnt lgkmcnt(0)
	v_add_f32_e32 v3, v3, v22
	ds_bpermute_b32 v8, v7, v3
	global_store_dwordx4 v[16:17], v[10:13], off offset:256
	s_and_saveexec_b64 s[10:11], s[38:39]
	s_cbranch_execz .LBB0_1167
	v_lshlrev_b64 v[4:5], 7, v[4:5]
	v_lshl_add_u64 v[4:5], s[50:51], 0, v[4:5]
	v_lshl_add_u64 v[4:5], s[8:9], 2, v[4:5]
	s_lshl_b32 s14, s17, 2
	s_mov_b32 s15, s60
	v_lshl_add_u64 v[4:5], v[4:5], 0, s[14:15]
	s_waitcnt lgkmcnt(0)
	v_add_f32_e32 v3, v3, v8
	global_store_dword v[4:5], v3, off
.LBB0_1167:
	s_or_b64 exec, exec, s[10:11]
	v_add_u32_e32 v4, s12, v172
	v_ashrrev_i32_e32 v5, 31, v4
	s_waitcnt lgkmcnt(0)
	v_lshlrev_b64 v[8:9], 12, v[4:5]
	v_lshl_add_u64 v[8:9], s[4:5], 0, v[8:9]
	v_lshl_add_u64 v[16:17], v[0:1], 1, v[8:9]
	s_nop 0
	s_mov_b32 s10, 0x3d000000
	s_waitcnt vmcnt(15)
	v_mov_b32_e32 v8, v206
	v_mov_b32_e32 v9, v207
	v_mov_b32_e32 v10, v208
	v_mov_b32_e32 v11, v209
	v_lshlrev_b32_e32 v12, 16, v8
	v_and_b32_e32 v13, 0xffff0000, v8
	v_lshlrev_b32_e32 v8, 16, v9
	v_and_b32_e32 v9, 0xffff0000, v9
	v_lshlrev_b32_e32 v14, 16, v10
	v_and_b32_e32 v15, 0xffff0000, v10
	v_lshlrev_b32_e32 v10, 16, v11
	v_and_b32_e32 v11, 0xffff0000, v11
	v_pk_fma_f32 v[18:19], v[110:111], s[10:11], v[8:9] op_sel_hi:[1,0,1]
	v_pk_fma_f32 v[20:21], v[108:109], s[10:11], v[12:13] op_sel_hi:[1,0,1]
	v_pk_fma_f32 v[22:23], v[106:107], s[10:11], v[10:11] op_sel_hi:[1,0,1]
	v_pk_fma_f32 v[24:25], v[104:105], s[10:11], v[14:15] op_sel_hi:[1,0,1]
	v_cvt_pk_bf16_f32 v8, v20, v21
	v_cvt_pk_bf16_f32 v9, v18, v19
	v_mul_f32_e32 v3, v21, v21
	v_cvt_pk_bf16_f32 v10, v24, v25
	v_cvt_pk_bf16_f32 v11, v22, v23
	s_nop 0
	v_mul_f32_e32 v19, v19, v19
	v_mul_f32_e32 v21, v25, v25
	v_fmac_f32_e32 v3, v20, v20
	v_fmac_f32_e32 v19, v18, v18
	v_mul_f32_e32 v23, v23, v23
	v_fmac_f32_e32 v21, v24, v24
	v_add_f32_e32 v3, v3, v19
	v_fmac_f32_e32 v23, v22, v22
	v_add_f32_e32 v3, v21, v3
	v_add_f32_e32 v3, v23, v3
	global_store_dwordx4 v[16:17], v[8:11], off
	s_waitcnt vmcnt(15)
	v_mov_b32_e32 v12, v210
	v_mov_b32_e32 v13, v211
	v_mov_b32_e32 v14, v212
	v_mov_b32_e32 v15, v213
	v_lshlrev_b32_e32 v18, 16, v12
	v_and_b32_e32 v19, 0xffff0000, v12
	v_lshlrev_b32_e32 v12, 16, v13
	v_and_b32_e32 v13, 0xffff0000, v13
	v_lshlrev_b32_e32 v20, 16, v14
	v_and_b32_e32 v21, 0xffff0000, v14
	v_pk_fma_f32 v[12:13], v[102:103], s[10:11], v[12:13] op_sel_hi:[1,0,1]
	v_pk_fma_f32 v[18:19], v[100:101], s[10:11], v[18:19] op_sel_hi:[1,0,1]
	v_lshlrev_b32_e32 v14, 16, v15
	v_and_b32_e32 v15, 0xffff0000, v15
	v_pk_fma_f32 v[20:21], v[96:97], s[10:11], v[20:21] op_sel_hi:[1,0,1]
	v_mul_f32_e32 v22, v19, v19
	v_mul_f32_e32 v23, v13, v13
	v_pk_fma_f32 v[14:15], v[98:99], s[10:11], v[14:15] op_sel_hi:[1,0,1]
	v_mul_f32_e32 v24, v21, v21
	v_fmac_f32_e32 v22, v18, v18
	v_fmac_f32_e32 v23, v12, v12
	v_mul_f32_e32 v25, v15, v15
	v_fmac_f32_e32 v24, v20, v20
	v_add_f32_e32 v22, v22, v23
	v_add_f32_e32 v22, v24, v22
	v_fmac_f32_e32 v25, v14, v14
	v_add_f32_e32 v22, v25, v22
	v_add_f32_e32 v3, v3, v22
	ds_bpermute_b32 v22, v6, v3
	v_cvt_pk_bf16_f32 v10, v18, v19
	v_cvt_pk_bf16_f32 v11, v12, v13
	v_cvt_pk_bf16_f32 v12, v20, v21
	v_cvt_pk_bf16_f32 v13, v14, v15
	s_waitcnt lgkmcnt(0)
	v_add_f32_e32 v3, v3, v22
	ds_bpermute_b32 v8, v7, v3
	global_store_dwordx4 v[16:17], v[10:13], off offset:256
	s_and_saveexec_b64 s[10:11], s[38:39]
	s_cbranch_execz .LBB0_1169
	v_lshlrev_b64 v[4:5], 7, v[4:5]
	v_lshl_add_u64 v[4:5], s[50:51], 0, v[4:5]
	v_lshl_add_u64 v[4:5], s[8:9], 2, v[4:5]
	s_lshl_b32 s12, s17, 2
	s_mov_b32 s13, s60
	v_lshl_add_u64 v[4:5], v[4:5], 0, s[12:13]
	s_waitcnt lgkmcnt(0)
	v_add_f32_e32 v3, v3, v8
	global_store_dword v[4:5], v3, off
.LBB0_1169:
	s_or_b64 exec, exec, s[10:11]
	v_add_u32_e32 v4, 0x80, v2
	v_ashrrev_i32_e32 v5, 31, v4
	s_waitcnt lgkmcnt(0)
	v_lshlrev_b64 v[8:9], 12, v[4:5]
	v_lshl_add_u64 v[8:9], s[4:5], 0, v[8:9]
	v_lshl_add_u64 v[16:17], v[0:1], 1, v[8:9]
	s_nop 0
	s_mov_b32 s10, 0x3d000000
	s_waitcnt vmcnt(15)
	v_mov_b32_e32 v8, v224
	v_mov_b32_e32 v9, v225
	v_mov_b32_e32 v10, v226
	v_mov_b32_e32 v11, v227
	v_lshlrev_b32_e32 v12, 16, v8
	v_and_b32_e32 v13, 0xffff0000, v8
	v_lshlrev_b32_e32 v8, 16, v9
	v_and_b32_e32 v9, 0xffff0000, v9
	v_lshlrev_b32_e32 v14, 16, v10
	v_and_b32_e32 v15, 0xffff0000, v10
	v_lshlrev_b32_e32 v10, 16, v11
	v_and_b32_e32 v11, 0xffff0000, v11
	v_pk_fma_f32 v[18:19], v[94:95], s[10:11], v[8:9] op_sel_hi:[1,0,1]
	v_pk_fma_f32 v[20:21], v[92:93], s[10:11], v[12:13] op_sel_hi:[1,0,1]
	v_pk_fma_f32 v[22:23], v[90:91], s[10:11], v[10:11] op_sel_hi:[1,0,1]
	v_pk_fma_f32 v[24:25], v[88:89], s[10:11], v[14:15] op_sel_hi:[1,0,1]
	v_cvt_pk_bf16_f32 v8, v20, v21
	v_cvt_pk_bf16_f32 v9, v18, v19
	v_mul_f32_e32 v3, v21, v21
	v_cvt_pk_bf16_f32 v10, v24, v25
	v_cvt_pk_bf16_f32 v11, v22, v23
	s_nop 0
	v_mul_f32_e32 v19, v19, v19
	v_mul_f32_e32 v21, v25, v25
	v_fmac_f32_e32 v3, v20, v20
	v_fmac_f32_e32 v19, v18, v18
	v_mul_f32_e32 v23, v23, v23
	v_fmac_f32_e32 v21, v24, v24
	v_add_f32_e32 v3, v3, v19
	v_fmac_f32_e32 v23, v22, v22
	v_add_f32_e32 v3, v21, v3
	v_add_f32_e32 v3, v23, v3
	global_store_dwordx4 v[16:17], v[8:11], off
	s_waitcnt vmcnt(15)
	v_mov_b32_e32 v12, v228
	v_mov_b32_e32 v13, v229
	v_mov_b32_e32 v14, v230
	v_mov_b32_e32 v15, v231
	v_lshlrev_b32_e32 v18, 16, v12
	v_and_b32_e32 v19, 0xffff0000, v12
	v_lshlrev_b32_e32 v12, 16, v13
	v_and_b32_e32 v13, 0xffff0000, v13
	v_lshlrev_b32_e32 v20, 16, v14
	v_and_b32_e32 v21, 0xffff0000, v14
	v_pk_fma_f32 v[12:13], v[86:87], s[10:11], v[12:13] op_sel_hi:[1,0,1]
	v_pk_fma_f32 v[18:19], v[84:85], s[10:11], v[18:19] op_sel_hi:[1,0,1]
	v_lshlrev_b32_e32 v14, 16, v15
	v_and_b32_e32 v15, 0xffff0000, v15
	v_pk_fma_f32 v[20:21], v[80:81], s[10:11], v[20:21] op_sel_hi:[1,0,1]
	v_mul_f32_e32 v22, v19, v19
	v_mul_f32_e32 v23, v13, v13
	v_pk_fma_f32 v[14:15], v[82:83], s[10:11], v[14:15] op_sel_hi:[1,0,1]
	v_mul_f32_e32 v24, v21, v21
	v_fmac_f32_e32 v22, v18, v18
	v_fmac_f32_e32 v23, v12, v12
	v_mul_f32_e32 v25, v15, v15
	v_fmac_f32_e32 v24, v20, v20
	v_add_f32_e32 v22, v22, v23
	v_add_f32_e32 v22, v24, v22
	v_fmac_f32_e32 v25, v14, v14
	v_add_f32_e32 v22, v25, v22
	v_add_f32_e32 v3, v3, v22
	ds_bpermute_b32 v22, v6, v3
	v_cvt_pk_bf16_f32 v10, v18, v19
	v_cvt_pk_bf16_f32 v11, v12, v13
	v_cvt_pk_bf16_f32 v12, v20, v21
	v_cvt_pk_bf16_f32 v13, v14, v15
	s_waitcnt lgkmcnt(0)
	v_add_f32_e32 v3, v3, v22
	ds_bpermute_b32 v8, v7, v3
	global_store_dwordx4 v[16:17], v[10:13], off offset:256
	s_and_saveexec_b64 s[10:11], s[38:39]
	s_cbranch_execz .LBB0_1171
	v_lshlrev_b64 v[4:5], 7, v[4:5]
	v_lshl_add_u64 v[4:5], s[50:51], 0, v[4:5]
	v_lshl_add_u64 v[4:5], s[8:9], 2, v[4:5]
	s_lshl_b32 s12, s17, 2
	s_mov_b32 s13, s60
	v_lshl_add_u64 v[4:5], v[4:5], 0, s[12:13]
	s_waitcnt lgkmcnt(0)
	v_add_f32_e32 v3, v3, v8
	global_store_dword v[4:5], v3, off
.LBB0_1171:
	s_or_b64 exec, exec, s[10:11]
	v_add_u32_e32 v4, 0x90, v2
	v_ashrrev_i32_e32 v5, 31, v4
	s_waitcnt lgkmcnt(0)
	v_lshlrev_b64 v[8:9], 12, v[4:5]
	v_lshl_add_u64 v[8:9], s[4:5], 0, v[8:9]
	v_lshl_add_u64 v[16:17], v[0:1], 1, v[8:9]
	s_nop 0
	s_mov_b32 s10, 0x3d000000
	s_waitcnt vmcnt(15)
	v_mov_b32_e32 v8, v236
	v_mov_b32_e32 v9, v237
	v_mov_b32_e32 v10, v238
	v_mov_b32_e32 v11, v239
	v_lshlrev_b32_e32 v12, 16, v8
	v_and_b32_e32 v13, 0xffff0000, v8
	v_lshlrev_b32_e32 v8, 16, v9
	v_and_b32_e32 v9, 0xffff0000, v9
	v_lshlrev_b32_e32 v14, 16, v10
	v_and_b32_e32 v15, 0xffff0000, v10
	v_lshlrev_b32_e32 v10, 16, v11
	v_and_b32_e32 v11, 0xffff0000, v11
	v_pk_fma_f32 v[18:19], v[78:79], s[10:11], v[8:9] op_sel_hi:[1,0,1]
	v_pk_fma_f32 v[20:21], v[76:77], s[10:11], v[12:13] op_sel_hi:[1,0,1]
	v_pk_fma_f32 v[22:23], v[74:75], s[10:11], v[10:11] op_sel_hi:[1,0,1]
	v_pk_fma_f32 v[24:25], v[72:73], s[10:11], v[14:15] op_sel_hi:[1,0,1]
	v_cvt_pk_bf16_f32 v8, v20, v21
	v_cvt_pk_bf16_f32 v9, v18, v19
	v_mul_f32_e32 v3, v21, v21
	v_cvt_pk_bf16_f32 v10, v24, v25
	v_cvt_pk_bf16_f32 v11, v22, v23
	s_nop 0
	v_mul_f32_e32 v19, v19, v19
	v_mul_f32_e32 v21, v25, v25
	v_fmac_f32_e32 v3, v20, v20
	v_fmac_f32_e32 v19, v18, v18
	v_mul_f32_e32 v23, v23, v23
	v_fmac_f32_e32 v21, v24, v24
	v_add_f32_e32 v3, v3, v19
	v_fmac_f32_e32 v23, v22, v22
	v_add_f32_e32 v3, v21, v3
	v_add_f32_e32 v3, v23, v3
	global_store_dwordx4 v[16:17], v[8:11], off
	s_waitcnt vmcnt(15)
	v_mov_b32_e32 v12, v240
	v_mov_b32_e32 v13, v241
	v_mov_b32_e32 v14, v242
	v_mov_b32_e32 v15, v243
	v_lshlrev_b32_e32 v18, 16, v12
	v_and_b32_e32 v19, 0xffff0000, v12
	v_lshlrev_b32_e32 v12, 16, v13
	v_and_b32_e32 v13, 0xffff0000, v13
	v_lshlrev_b32_e32 v20, 16, v14
	v_and_b32_e32 v21, 0xffff0000, v14
	v_pk_fma_f32 v[12:13], v[70:71], s[10:11], v[12:13] op_sel_hi:[1,0,1]
	v_pk_fma_f32 v[18:19], v[68:69], s[10:11], v[18:19] op_sel_hi:[1,0,1]
	v_lshlrev_b32_e32 v14, 16, v15
	v_and_b32_e32 v15, 0xffff0000, v15
	v_pk_fma_f32 v[20:21], v[64:65], s[10:11], v[20:21] op_sel_hi:[1,0,1]
	v_mul_f32_e32 v22, v19, v19
	v_mul_f32_e32 v23, v13, v13
	v_pk_fma_f32 v[14:15], v[66:67], s[10:11], v[14:15] op_sel_hi:[1,0,1]
	v_mul_f32_e32 v24, v21, v21
	v_fmac_f32_e32 v22, v18, v18
	v_fmac_f32_e32 v23, v12, v12
	v_mul_f32_e32 v25, v15, v15
	v_fmac_f32_e32 v24, v20, v20
	v_add_f32_e32 v22, v22, v23
	v_add_f32_e32 v22, v24, v22
	v_fmac_f32_e32 v25, v14, v14
	v_add_f32_e32 v22, v25, v22
	v_add_f32_e32 v3, v3, v22
	ds_bpermute_b32 v22, v6, v3
	v_cvt_pk_bf16_f32 v10, v18, v19
	v_cvt_pk_bf16_f32 v11, v12, v13
	v_cvt_pk_bf16_f32 v12, v20, v21
	v_cvt_pk_bf16_f32 v13, v14, v15
	s_waitcnt lgkmcnt(0)
	v_add_f32_e32 v3, v3, v22
	ds_bpermute_b32 v8, v7, v3
	global_store_dwordx4 v[16:17], v[10:13], off offset:256
	s_and_saveexec_b64 s[10:11], s[38:39]
	s_cbranch_execz .LBB0_1173
	v_lshlrev_b64 v[4:5], 7, v[4:5]
	v_lshl_add_u64 v[4:5], s[50:51], 0, v[4:5]
	v_lshl_add_u64 v[4:5], s[8:9], 2, v[4:5]
	s_lshl_b32 s12, s17, 2
	s_mov_b32 s13, s60
	v_lshl_add_u64 v[4:5], v[4:5], 0, s[12:13]
	s_waitcnt lgkmcnt(0)
	v_add_f32_e32 v3, v3, v8
	global_store_dword v[4:5], v3, off
.LBB0_1173:
	s_or_b64 exec, exec, s[10:11]
	v_add_u32_e32 v4, 0xa0, v2
	v_ashrrev_i32_e32 v5, 31, v4
	s_waitcnt lgkmcnt(0)
	v_lshlrev_b64 v[8:9], 12, v[4:5]
	v_lshl_add_u64 v[8:9], s[4:5], 0, v[8:9]
	v_lshl_add_u64 v[16:17], v[0:1], 1, v[8:9]
	s_nop 0
	s_mov_b32 s10, 0x3d000000
	s_waitcnt vmcnt(15)
	v_mov_b32_e32 v8, v244
	v_mov_b32_e32 v9, v245
	v_mov_b32_e32 v10, v246
	v_mov_b32_e32 v11, v247
	v_lshlrev_b32_e32 v12, 16, v8
	v_and_b32_e32 v13, 0xffff0000, v8
	v_lshlrev_b32_e32 v8, 16, v9
	v_and_b32_e32 v9, 0xffff0000, v9
	v_lshlrev_b32_e32 v14, 16, v10
	v_and_b32_e32 v15, 0xffff0000, v10
	v_lshlrev_b32_e32 v10, 16, v11
	v_and_b32_e32 v11, 0xffff0000, v11
	v_pk_fma_f32 v[18:19], v[62:63], s[10:11], v[8:9] op_sel_hi:[1,0,1]
	v_pk_fma_f32 v[20:21], v[60:61], s[10:11], v[12:13] op_sel_hi:[1,0,1]
	v_pk_fma_f32 v[22:23], v[58:59], s[10:11], v[10:11] op_sel_hi:[1,0,1]
	v_pk_fma_f32 v[24:25], v[56:57], s[10:11], v[14:15] op_sel_hi:[1,0,1]
	v_cvt_pk_bf16_f32 v8, v20, v21
	v_cvt_pk_bf16_f32 v9, v18, v19
	v_mul_f32_e32 v3, v21, v21
	v_cvt_pk_bf16_f32 v10, v24, v25
	v_cvt_pk_bf16_f32 v11, v22, v23
	s_nop 0
	v_mul_f32_e32 v19, v19, v19
	v_mul_f32_e32 v21, v25, v25
	v_fmac_f32_e32 v3, v20, v20
	v_fmac_f32_e32 v19, v18, v18
	v_mul_f32_e32 v23, v23, v23
	v_fmac_f32_e32 v21, v24, v24
	v_add_f32_e32 v3, v3, v19
	v_fmac_f32_e32 v23, v22, v22
	v_add_f32_e32 v3, v21, v3
	v_add_f32_e32 v3, v23, v3
	global_store_dwordx4 v[16:17], v[8:11], off
	s_waitcnt vmcnt(13)
	v_mov_b32_e32 v12, v144
	v_mov_b32_e32 v13, v145
	v_mov_b32_e32 v14, v146
	v_mov_b32_e32 v15, v147
	v_lshlrev_b32_e32 v18, 16, v12
	v_and_b32_e32 v19, 0xffff0000, v12
	v_lshlrev_b32_e32 v12, 16, v13
	v_and_b32_e32 v13, 0xffff0000, v13
	v_lshlrev_b32_e32 v20, 16, v14
	v_and_b32_e32 v21, 0xffff0000, v14
	v_pk_fma_f32 v[12:13], v[54:55], s[10:11], v[12:13] op_sel_hi:[1,0,1]
	v_pk_fma_f32 v[18:19], v[52:53], s[10:11], v[18:19] op_sel_hi:[1,0,1]
	v_lshlrev_b32_e32 v14, 16, v15
	v_and_b32_e32 v15, 0xffff0000, v15
	v_pk_fma_f32 v[20:21], v[48:49], s[10:11], v[20:21] op_sel_hi:[1,0,1]
	v_mul_f32_e32 v22, v19, v19
	v_mul_f32_e32 v23, v13, v13
	v_pk_fma_f32 v[14:15], v[50:51], s[10:11], v[14:15] op_sel_hi:[1,0,1]
	v_mul_f32_e32 v24, v21, v21
	v_fmac_f32_e32 v22, v18, v18
	v_fmac_f32_e32 v23, v12, v12
	v_mul_f32_e32 v25, v15, v15
	v_fmac_f32_e32 v24, v20, v20
	v_add_f32_e32 v22, v22, v23
	v_add_f32_e32 v22, v24, v22
	v_fmac_f32_e32 v25, v14, v14
	v_add_f32_e32 v22, v25, v22
	v_add_f32_e32 v3, v3, v22
	ds_bpermute_b32 v22, v6, v3
	v_cvt_pk_bf16_f32 v10, v18, v19
	v_cvt_pk_bf16_f32 v11, v12, v13
	v_cvt_pk_bf16_f32 v12, v20, v21
	v_cvt_pk_bf16_f32 v13, v14, v15
	s_waitcnt lgkmcnt(0)
	v_add_f32_e32 v3, v3, v22
	ds_bpermute_b32 v8, v7, v3
	global_store_dwordx4 v[16:17], v[10:13], off offset:256
	s_and_saveexec_b64 s[10:11], s[38:39]
	s_cbranch_execz .LBB0_1175
	v_lshlrev_b64 v[4:5], 7, v[4:5]
	v_lshl_add_u64 v[4:5], s[50:51], 0, v[4:5]
	v_lshl_add_u64 v[4:5], s[8:9], 2, v[4:5]
	s_lshl_b32 s12, s17, 2
	s_mov_b32 s13, s60
	v_lshl_add_u64 v[4:5], v[4:5], 0, s[12:13]
	s_waitcnt lgkmcnt(0)
	v_add_f32_e32 v3, v3, v8
	global_store_dword v[4:5], v3, off
.LBB0_1175:
	s_or_b64 exec, exec, s[10:11]
	v_add_u32_e32 v2, 0xb0, v2
	v_ashrrev_i32_e32 v3, 31, v2
	v_lshlrev_b64 v[4:5], 12, v[2:3]
	v_lshl_add_u64 v[4:5], s[4:5], 0, v[4:5]
	v_lshl_add_u64 v[16:17], v[0:1], 1, v[4:5]
	s_waitcnt lgkmcnt(0)
	s_nop 0
	s_mov_b32 s10, 0x3d000000
	s_waitcnt vmcnt(13)
	v_mov_b32_e32 v8, v148
	v_mov_b32_e32 v9, v149
	v_mov_b32_e32 v10, v150
	v_mov_b32_e32 v11, v151
	v_lshlrev_b32_e32 v0, 16, v8
	v_and_b32_e32 v1, 0xffff0000, v8
	v_lshlrev_b32_e32 v4, 16, v9
	v_and_b32_e32 v5, 0xffff0000, v9
	v_lshlrev_b32_e32 v8, 16, v10
	v_and_b32_e32 v9, 0xffff0000, v10
	v_lshlrev_b32_e32 v10, 16, v11
	v_and_b32_e32 v11, 0xffff0000, v11
	v_pk_fma_f32 v[4:5], v[46:47], s[10:11], v[4:5] op_sel_hi:[1,0,1]
	v_pk_fma_f32 v[0:1], v[44:45], s[10:11], v[0:1] op_sel_hi:[1,0,1]
	v_pk_fma_f32 v[18:19], v[42:43], s[10:11], v[10:11] op_sel_hi:[1,0,1]
	v_pk_fma_f32 v[20:21], v[40:41], s[10:11], v[8:9] op_sel_hi:[1,0,1]
	v_cvt_pk_bf16_f32 v8, v0, v1
	v_cvt_pk_bf16_f32 v9, v4, v5
	v_mul_f32_e32 v1, v1, v1
	v_cvt_pk_bf16_f32 v10, v20, v21
	v_cvt_pk_bf16_f32 v11, v18, v19
	s_nop 0
	v_mul_f32_e32 v5, v5, v5
	v_mul_f32_e32 v21, v21, v21
	v_fmac_f32_e32 v1, v0, v0
	v_fmac_f32_e32 v5, v4, v4
	v_mul_f32_e32 v19, v19, v19
	v_fmac_f32_e32 v21, v20, v20
	v_add_f32_e32 v0, v1, v5
	v_fmac_f32_e32 v19, v18, v18
	v_add_f32_e32 v0, v21, v0
	v_add_f32_e32 v20, v19, v0
	global_store_dwordx4 v[16:17], v[8:11], off
	s_waitcnt vmcnt(13)
	v_mov_b32_e32 v12, v152
	v_mov_b32_e32 v13, v153
	v_mov_b32_e32 v14, v154
	v_mov_b32_e32 v15, v155
	v_lshlrev_b32_e32 v0, 16, v12
	v_and_b32_e32 v1, 0xffff0000, v12
	v_lshlrev_b32_e32 v4, 16, v13
	v_and_b32_e32 v5, 0xffff0000, v13
	v_lshlrev_b32_e32 v12, 16, v14
	v_and_b32_e32 v13, 0xffff0000, v14
	v_pk_fma_f32 v[18:19], v[38:39], s[10:11], v[4:5] op_sel_hi:[1,0,1]
	v_pk_fma_f32 v[0:1], v[36:37], s[10:11], v[0:1] op_sel_hi:[1,0,1]
	v_lshlrev_b32_e32 v14, 16, v15
	v_and_b32_e32 v15, 0xffff0000, v15
	v_pk_fma_f32 v[12:13], v[32:33], s[10:11], v[12:13] op_sel_hi:[1,0,1]
	v_mul_f32_e32 v4, v1, v1
	v_mul_f32_e32 v5, v19, v19
	v_pk_fma_f32 v[14:15], v[34:35], s[10:11], v[14:15] op_sel_hi:[1,0,1]
	v_mul_f32_e32 v21, v13, v13
	v_fmac_f32_e32 v4, v0, v0
	v_fmac_f32_e32 v5, v18, v18
	v_mul_f32_e32 v22, v15, v15
	v_fmac_f32_e32 v21, v12, v12
	v_add_f32_e32 v4, v4, v5
	v_add_f32_e32 v4, v21, v4
	v_fmac_f32_e32 v22, v14, v14
	v_add_f32_e32 v4, v22, v4
	v_add_f32_e32 v5, v20, v4
	ds_bpermute_b32 v6, v6, v5
	v_cvt_pk_bf16_f32 v4, v0, v1
	s_waitcnt lgkmcnt(0)
	v_add_f32_e32 v0, v5, v6
	ds_bpermute_b32 v1, v7, v0
	v_cvt_pk_bf16_f32 v5, v18, v19
	v_cvt_pk_bf16_f32 v6, v12, v13
	v_cvt_pk_bf16_f32 v7, v14, v15
	global_store_dwordx4 v[16:17], v[4:7], off offset:256
	s_and_saveexec_b64 s[10:11], s[38:39]
	s_cbranch_execz .LBB0_1177
	v_lshlrev_b64 v[2:3], 7, v[2:3]
	v_lshl_add_u64 v[2:3], s[50:51], 0, v[2:3]
	v_lshl_add_u64 v[2:3], s[8:9], 2, v[2:3]
	s_lshl_b32 s8, s17, 2
	s_mov_b32 s9, s60
	v_lshl_add_u64 v[2:3], v[2:3], 0, s[8:9]
	s_waitcnt lgkmcnt(0)
	v_add_f32_e32 v0, v0, v1
	global_store_dword v[2:3], v0, off
